# retention core: LDS-DMA issue of k-steps 0-3 and the first V-step moved behind the step's ds_read_b128 group
# speedup vs baseline: 1.0049x; 1.0049x over previous
; template <int VAR  >
; __device__ __forceinline__ void ret_core_mfma(const bf16* P, const bf16* VT, const float* decay_logit  , bf16* YF, bf16* YB, float* PT, LAS unsigned char* lds, const int tid, const int bid, const int G) {
;     ...
;             for (int js = 0; js < 4; ++js) { const v4u kw = vnx[js]; float kd[8];
;                 { const LAS f32x4* kp = (const LAS f32x4*)(lds + RC_TB + (32 * js + 8 * fqc) * 4); const f32x4 k0 = kp[0], k1 = kp[1];
;                   kd[0] = k0[0]; kd[1] = k0[1]; kd[2] = k0[2]; kd[3] = k0[3]; kd[4] = k1[0]; kd[5] = k1[1]; kd[6] = k1[2]; kd[7] = k1[3]; }
;                 v4u sw; sw.x = cvtpk(bflo(kw.x) * kd[0], bfhi(kw.x) * kd[1]); sw.y = cvtpk(bflo(kw.y) * kd[2], bfhi(kw.y) * kd[3]); sw.z = cvtpk(bflo(kw.z) * kd[4], bfhi(kw.z) * kd[5]); sw.w = cvtpk(bflo(kw.w) * kd[6], bfhi(kw.w) * kd[7]);
;                 Avs[js] = __builtin_bit_cast(bf16x8v, sw); }
; #pragma unroll
;             for (int n = 0; n < 16; ++n) acc4[n] = acc4[n] * cdec;
;             const int jj = 8 * fqc + (frc >> 2);
;             const unsigned trA = (unsigned)((jj >> 4) * 1024 + sl_swz((jj & 15) * 64 + 8 * (frc & 3))), trB = (unsigned)(((jj + 4) >> 4) * 1024 + sl_swz(((jj + 4) & 15) * 64 + 8 * (frc & 3)));
;             f32x4 accA[4][2], accY[4][2];
; #pragma unroll
;             for (int m = 0; m < 4; ++m)
; #pragma unroll
;                 for (int n = 0; n < 2; ++n) { accA[m][n] = (f32x4){0.f, 0.f, 0.f, 0.f}; accY[m][n] = (f32x4){0.f, 0.f, 0.f, 0.f}; }
; #pragma unroll
;             for (int ks = 0; ks < 8; ++ks) {
;                 if (ks < 4) { if (c == 0) RC_WAITV(6); else RC_WAITV(14); } else if (ks == 4) RC_WAITV(6); else if (ks == 5) RC_WAITV(5); else if (ks == 6) RC_WAITV(4); else RC_WAITV(3);
;                 RC_BAR();
;                 { const int s4 = RC_PREV(slot);
;                   if (ks + 4 < 12) RC_ISSUE(ks + 4, tok0, s4); else RC_ISSUE(ks + 4 - 12, tokn, s4); }
;                 bf16x8v At[4], Bk[2], Bs[2];
;                 const LAS unsigned char* sq = lds + RC_RG + slot * 16384;
; #pragma unroll
;                 for (int m = 0; m < 4; ++m) At[m] = *(const LAS bf16x8v*)(sq + aoff + m * 1024);
; #pragma unroll
;                 for (int n = 0; n < 2; ++n) { Bk[n] = *(const LAS bf16x8v*)(sq + 8192 + boff + n * 1024); Bs[n] = *(const LAS bf16x8v*)(lds + RC_ST + ks * 8192 + boff + n * 1024); }
; #pragma unroll
.LBB0_46:
	v_lshlrev_b32_e32 v116, 16, v88
	v_and_b32_e32 v117, 0xffff0000, v88
	v_lshlrev_b32_e32 v88, 16, v89
	v_and_b32_e32 v89, 0xffff0000, v89
	s_waitcnt lgkmcnt(0)
	v_pk_mul_f32 v[68:69], v[68:69], v[116:117]
	v_pk_mul_f32 v[70:71], v[70:71], v[88:89]
	v_cvt_pk_bf16_f32 v68, v68, v69
	v_cvt_pk_bf16_f32 v69, v70, v71
	v_lshlrev_b32_e32 v70, 16, v90
	v_and_b32_e32 v71, 0xffff0000, v90
	v_lshlrev_b32_e32 v88, 16, v91
	v_and_b32_e32 v89, 0xffff0000, v91
	v_pk_mul_f32 v[70:71], v[112:113], v[70:71]
	v_pk_mul_f32 v[88:89], v[114:115], v[88:89]
	v_cvt_pk_bf16_f32 v70, v70, v71
	v_cvt_pk_bf16_f32 v71, v88, v89
	v_lshlrev_b32_e32 v88, 16, v84
	v_and_b32_e32 v89, 0xffff0000, v84
	v_lshlrev_b32_e32 v84, 16, v85
	v_and_b32_e32 v85, 0xffff0000, v85
	v_pk_mul_f32 v[72:73], v[72:73], v[88:89]
	v_pk_mul_f32 v[74:75], v[74:75], v[84:85]
	v_cvt_pk_bf16_f32 v72, v72, v73
	v_cvt_pk_bf16_f32 v73, v74, v75
	v_lshlrev_b32_e32 v74, 16, v86
	v_and_b32_e32 v75, 0xffff0000, v86
	v_lshlrev_b32_e32 v84, 16, v87
	v_and_b32_e32 v85, 0xffff0000, v87
	v_pk_mul_f32 v[74:75], v[108:109], v[74:75]
	v_pk_mul_f32 v[84:85], v[110:111], v[84:85]
	v_cvt_pk_bf16_f32 v74, v74, v75
	v_cvt_pk_bf16_f32 v75, v84, v85
	v_lshlrev_b32_e32 v84, 16, v76
	v_and_b32_e32 v85, 0xffff0000, v76
	v_pk_mul_f32 v[84:85], v[104:105], v[84:85]
	s_add_i32 s38, s39, 1
	v_cvt_pk_bf16_f32 v76, v84, v85
	v_lshlrev_b32_e32 v84, 16, v77
	v_and_b32_e32 v85, 0xffff0000, v77
	v_pk_mul_f32 v[84:85], v[106:107], v[84:85]
	v_lshlrev_b32_e32 v226, 3, v215
	v_cvt_pk_bf16_f32 v77, v84, v85
	v_lshlrev_b32_e32 v84, 16, v78
	v_and_b32_e32 v85, 0xffff0000, v78
	v_pk_mul_f32 v[84:85], v[100:101], v[84:85]
	v_bfe_u32 v2, v230, 2, 2
	v_cvt_pk_bf16_f32 v78, v84, v85
	v_lshlrev_b32_e32 v84, 16, v79
	v_and_b32_e32 v85, 0xffff0000, v79
	v_pk_mul_f32 v[84:85], v[102:103], v[84:85]
	s_and_b64 s[6:7], s[4:5], exec
	v_cvt_pk_bf16_f32 v79, v84, v85
	v_lshlrev_b32_e32 v84, 16, v80
	v_and_b32_e32 v85, 0xffff0000, v80
	v_pk_mul_f32 v[84:85], v[96:97], v[84:85]
	v_or_b32_e32 v2, v226, v2
	v_cvt_pk_bf16_f32 v80, v84, v85
	v_lshlrev_b32_e32 v84, 16, v81
	v_and_b32_e32 v85, 0xffff0000, v81
	v_pk_mul_f32 v[84:85], v[98:99], v[84:85]
	v_and_b32_e32 v213, 3, v230
	v_cvt_pk_bf16_f32 v81, v84, v85
	v_lshlrev_b32_e32 v84, 16, v82
	v_and_b32_e32 v85, 0xffff0000, v82
	v_pk_mul_f32 v[84:85], v[92:93], v[84:85]
	v_lshlrev_b32_e32 v2, 6, v2
	v_cvt_pk_bf16_f32 v82, v84, v85
	v_lshlrev_b32_e32 v84, 16, v83
	v_and_b32_e32 v85, 0xffff0000, v83
	v_pk_mul_f32 v[84:85], v[94:95], v[84:85]
	s_movk_i32 s6, 0x2c0
	v_cvt_pk_bf16_f32 v83, v84, v85
	v_lshlrev_b32_e32 v84, 5, v230
	v_lshlrev_b32_e32 v85, 3, v213
	s_cselect_b32 s38, s33, s38
	v_and_b32_e32 v84, 0xfffffc00, v84
	v_and_or_b32 v2, v2, s6, v85
	v_lshlrev_b32_e32 v85, 5, v215
	v_and_or_b32 v84, v85, 32, v84
	s_movk_i32 s6, 0x120
	s_lshl_b32 s60, s38, 19
	v_bitop3_b32 v229, v84, s6, v2 bitop3:0x36
	v_lshl_add_u64 v[232:233], v[218:219], 0, s[60:61]
	s_mov_b64 s[6:7], 0x100
	s_lshl_b32 s40, s52, 14
	v_or_b32_e32 v234, v84, v2
	v_bitop3_b32 v227, v84, 32, v2 bitop3:0x36
	v_lshl_add_u64 v[84:85], v[232:233], 0, s[6:7]
	s_add_i32 s6, s40, 0xffffc000
	s_cmp_lg_u32 s52, 0
	s_cselect_b32 s6, s6, 0x10000
	s_add_i32 s6, s6, 0
	s_add_i32 s41, s6, s44
	s_barrier
	s_add_i32 s6, s40, 0
	s_add_i32 s7, s6, 0x10000
	v_add_u32_e32 v236, 0, v243
	v_add_u32_e32 v2, s7, v242
	ds_read_b128 v[144:147], v236 offset:1024
	ds_read_b128 v[136:139], v236
	ds_read_b128 v[96:99], v2
	ds_read_b128 v[112:115], v2 offset:1024
	ds_read_b128 v[128:131], v2 offset:2048
	ds_read_b128 v[148:151], v2 offset:3072
	v_add_u32_e32 v2, s7, v243
	ds_read_b128 v[132:135], v2 offset:8192
	ds_read_b128 v[140:143], v2 offset:9216
	s_add_i32 m0, s41, 0x10000
	s_mov_b64 s[98:99], 0x900
	global_load_lds_dwordx4 v[84:85], off
	v_lshl_add_u64 v[84:85], v[232:233], 0, s[98:99]
	s_add_i32 m0, s41, 0x12000
	s_nop 0
	global_load_lds_dwordx4 v[84:85], off
	v_mov_b32_e32 v217, v216
	v_pk_mul_f32 v[42:43], v[216:217], v[42:43]
	v_pk_mul_f32 v[40:41], v[224:225], v[40:41]
	v_pk_mul_f32 v[38:39], v[216:217], v[38:39]
	v_pk_mul_f32 v[36:37], v[224:225], v[36:37]
	v_or_b32_e32 v231, 0x100, v234
	s_add_i32 s6, s6, 0x12000
	s_waitcnt lgkmcnt(0)
	v_mfma_f32_16x16x32_bf16 v[84:87], v[132:135], v[96:99], 0
	v_add_u32_e32 v2, s6, v234
	v_add_u32_e32 v180, s6, v231
	v_add_u32_e32 v181, s6, v227
	v_mfma_f32_16x16x32_bf16 v[88:91], v[136:139], v[96:99], 0
	v_add_u32_e32 v182, s6, v229
	s_andn2_b64 vcc, exec, s[0:1]
	v_mfma_f32_16x16x32_bf16 v[92:95], v[140:143], v[96:99], 0
	v_mfma_f32_16x16x32_bf16 v[96:99], v[144:147], v[96:99], 0
	v_mfma_f32_16x16x32_bf16 v[100:103], v[132:135], v[112:115], 0
	v_mfma_f32_16x16x32_bf16 v[104:107], v[136:139], v[112:115], 0
	v_mfma_f32_16x16x32_bf16 v[108:111], v[140:143], v[112:115], 0
	v_mfma_f32_16x16x32_bf16 v[112:115], v[144:147], v[112:115], 0
	v_mfma_f32_16x16x32_bf16 v[116:119], v[132:135], v[128:131], 0
	v_mfma_f32_16x16x32_bf16 v[120:123], v[136:139], v[128:131], 0
	v_mfma_f32_16x16x32_bf16 v[124:127], v[140:143], v[128:131], 0
	v_mfma_f32_16x16x32_bf16 v[128:131], v[144:147], v[128:131], 0
	v_mfma_f32_16x16x32_bf16 v[132:135], v[132:135], v[148:151], 0
	v_mfma_f32_16x16x32_bf16 v[136:139], v[136:139], v[148:151], 0
	v_mfma_f32_16x16x32_bf16 v[140:143], v[140:143], v[148:151], 0
	v_mfma_f32_16x16x32_bf16 v[144:147], v[144:147], v[148:151], 0
	ds_read_b64_tr_b16 v[176:177], v2
	ds_read_b64_tr_b16 v[178:179], v180
	ds_read_b64_tr_b16 v[172:173], v181
	ds_read_b64_tr_b16 v[174:175], v182
	ds_read_b64_tr_b16 v[168:169], v2 offset:2048
	ds_read_b64_tr_b16 v[170:171], v180 offset:2048
	ds_read_b64_tr_b16 v[164:165], v181 offset:2048
	ds_read_b64_tr_b16 v[166:167], v182 offset:2048
	ds_read_b64_tr_b16 v[160:161], v2 offset:4096
	ds_read_b64_tr_b16 v[162:163], v180 offset:4096
	ds_read_b64_tr_b16 v[156:157], v181 offset:4096
	ds_read_b64_tr_b16 v[158:159], v182 offset:4096
	ds_read_b64_tr_b16 v[152:153], v2 offset:6144
	ds_read_b64_tr_b16 v[154:155], v180 offset:6144
	ds_read_b64_tr_b16 v[148:149], v181 offset:6144
	ds_read_b64_tr_b16 v[150:151], v182 offset:6144
	s_waitcnt lgkmcnt(0)
	v_cndmask_b32_e64 v2, 0, 1, s[0:1]
	v_cmp_ne_u32_e64 s[6:7], 1, v2
	v_mfma_f32_16x16x32_bf16 v[40:43], v[176:179], v[68:71], v[40:43]
	v_mfma_f32_16x16x32_bf16 v[36:39], v[172:175], v[68:71], v[36:39]
	v_mfma_f32_16x16x32_bf16 v[40:43], v[168:171], v[72:75], v[40:43]
	v_mfma_f32_16x16x32_bf16 v[36:39], v[164:167], v[72:75], v[36:39]
	v_mfma_f32_16x16x32_bf16 v[40:43], v[160:163], v[76:79], v[40:43]
	v_mfma_f32_16x16x32_bf16 v[36:39], v[156:159], v[76:79], v[36:39]
	v_mfma_f32_16x16x32_bf16 v[40:43], v[152:155], v[80:83], v[40:43]
	v_mfma_f32_16x16x32_bf16 v[36:39], v[148:151], v[80:83], v[36:39]
	s_cbranch_vccnz .LBB0_64
	s_waitcnt vmcnt(14)
	s_cbranch_execnz .LBB0_49

; template <int VAR  >
; __device__ __forceinline__ void ret_core_mfma(const bf16* P, const bf16* VT, const float* decay_logit  , bf16* YF, bf16* YB, float* PT, LAS unsigned char* lds, const int tid, const int bid, const int G) {
;     ...
;             for (int ks = 0; ks < 8; ++ks) {
;                 if (ks < 4) { if (c == 0) RC_WAITV(6); else RC_WAITV(14); } else if (ks == 4) RC_WAITV(6); else if (ks == 5) RC_WAITV(5); else if (ks == 6) RC_WAITV(4); else RC_WAITV(3);
;                 RC_BAR();
;                 { const int s4 = RC_PREV(slot);
;                   if (ks + 4 < 12) RC_ISSUE(ks + 4, tok0, s4); else RC_ISSUE(ks + 4 - 12, tokn, s4); }
;                 bf16x8v At[4], Bk[2], Bs[2];
;                 const LAS unsigned char* sq = lds + RC_RG + slot * 16384;
; #pragma unroll
;                 for (int m = 0; m < 4; ++m) At[m] = *(const LAS bf16x8v*)(sq + aoff + m * 1024);
; #pragma unroll
;                 for (int n = 0; n < 2; ++n) { Bk[n] = *(const LAS bf16x8v*)(sq + 8192 + boff + n * 1024); Bs[n] = *(const LAS bf16x8v*)(lds + RC_ST + ks * 8192 + boff + n * 1024); }
; #pragma unroll
;                 for (int m = 0; m < 4; ++m)
; #pragma unroll
;                     for (int n = 0; n < 2; ++n) { accA[m][n] = RC_MFMA(Bk[n], At[m], accA[m][n]); accY[m][n] = RC_MFMA(Bs[n], At[m], accY[m][n]); }
;                 { const unsigned kb = (unsigned)(size_t)(sq + 8192);
;                   const unsigned a0 = kb + trA, a1 = kb + trB, b0 = kb + (trA ^ 32u), b1 = kb + (trB ^ 32u);
;                   v2u l0, h0, l1, h1, l2, h2, l3, h3, p0, q0, p1, q1, p2, q2, p3, q3;
;                   asm volatile("ds_read_b64_tr_b16 %0, %16\n\tds_read_b64_tr_b16 %1, %17\n\tds_read_b64_tr_b16 %8, %18\n\tds_read_b64_tr_b16 %9, %19\n\t"
;                                "ds_read_b64_tr_b16 %2, %16 offset:2048\n\tds_read_b64_tr_b16 %3, %17 offset:2048\n\tds_read_b64_tr_b16 %10, %18 offset:2048\n\tds_read_b64_tr_b16 %11, %19 offset:2048\n\t"
;                                "ds_read_b64_tr_b16 %4, %16 offset:4096\n\tds_read_b64_tr_b16 %5, %17 offset:4096\n\tds_read_b64_tr_b16 %12, %18 offset:4096\n\tds_read_b64_tr_b16 %13, %19 offset:4096\n\t"
;                                "ds_read_b64_tr_b16 %6, %16 offset:6144\n\tds_read_b64_tr_b16 %7, %17 offset:6144\n\tds_read_b64_tr_b16 %14, %18 offset:6144\n\tds_read_b64_tr_b16 %15, %19 offset:6144\n\ts_waitcnt lgkmcnt(0)"
.LBB0_49:
	s_add_i32 s0, s52, 1
	s_cmp_lg_u32 s52, 4
	s_cselect_b32 s40, s0, 0
	s_mov_b64 s[0:1], 0x140
	s_lshl_b32 s41, s40, 14
	v_lshl_add_u64 v[152:153], v[232:233], 0, s[0:1]
	s_add_i32 s0, s41, 0xffffc000
	s_cmp_lg_u32 s40, 0
	s_cselect_b32 s0, s0, 0x10000
	s_add_i32 s0, s0, 0
	s_add_i32 s42, s0, s44
	s_barrier
	s_add_i32 s0, s41, 0
	s_add_i32 s1, s0, 0x10000
	v_add_u32_e32 v2, s1, v242
	ds_read_b128 v[196:199], v236 offset:9216
	ds_read_b128 v[188:191], v236 offset:8192
	ds_read_b128 v[148:151], v2
	ds_read_b128 v[164:167], v2 offset:1024
	ds_read_b128 v[180:183], v2 offset:2048
	ds_read_b128 v[202:205], v2 offset:3072
	v_add_u32_e32 v2, s1, v243
	ds_read_b128 v[184:187], v2 offset:8192
	ds_read_b128 v[192:195], v2 offset:9216
	s_add_i32 m0, s42, 0x10000
	s_mov_b64 s[98:99], 0x940
	global_load_lds_dwordx4 v[152:153], off
	v_lshl_add_u64 v[152:153], v[232:233], 0, s[98:99]
	s_add_i32 m0, s42, 0x12000
	s_nop 0
	global_load_lds_dwordx4 v[152:153], off
	v_mov_b32_e32 v217, v216
	v_pk_mul_f32 v[18:19], v[216:217], v[18:19]
	v_pk_mul_f32 v[16:17], v[224:225], v[16:17]
	v_pk_mul_f32 v[14:15], v[216:217], v[14:15]
	v_pk_mul_f32 v[12:13], v[224:225], v[12:13]
	s_add_i32 s0, s0, 0x12000
	s_waitcnt lgkmcnt(0)
	v_mfma_f32_16x16x32_bf16 v[84:87], v[184:187], v[148:151], v[84:87]
	v_add_u32_e32 v2, s0, v234
	s_and_b64 vcc, exec, s[6:7]
	v_mfma_f32_16x16x32_bf16 v[88:91], v[188:191], v[148:151], v[88:91]
	v_mfma_f32_16x16x32_bf16 v[92:95], v[192:195], v[148:151], v[92:95]
	v_mfma_f32_16x16x32_bf16 v[148:151], v[196:199], v[148:151], v[96:99]
	v_mfma_f32_16x16x32_bf16 v[152:155], v[184:187], v[164:167], v[100:103]
	v_mfma_f32_16x16x32_bf16 v[156:159], v[188:191], v[164:167], v[104:107]
	v_mfma_f32_16x16x32_bf16 v[160:163], v[192:195], v[164:167], v[108:111]
	v_mfma_f32_16x16x32_bf16 v[164:167], v[196:199], v[164:167], v[112:115]
	v_mfma_f32_16x16x32_bf16 v[168:171], v[184:187], v[180:183], v[116:119]
	v_mfma_f32_16x16x32_bf16 v[172:175], v[188:191], v[180:183], v[120:123]
	v_mfma_f32_16x16x32_bf16 v[176:179], v[192:195], v[180:183], v[124:127]
	v_mfma_f32_16x16x32_bf16 v[180:183], v[196:199], v[180:183], v[128:131]
	s_nop 2
	v_add_u32_e32 v128, s0, v231
	v_add_u32_e32 v129, s0, v227
	v_add_u32_e32 v130, s0, v229
	ds_read_b64_tr_b16 v[124:125], v2
	ds_read_b64_tr_b16 v[126:127], v128
	ds_read_b64_tr_b16 v[120:121], v129
	ds_read_b64_tr_b16 v[122:123], v130
	ds_read_b64_tr_b16 v[116:117], v2 offset:2048
	ds_read_b64_tr_b16 v[118:119], v128 offset:2048
	ds_read_b64_tr_b16 v[112:113], v129 offset:2048
	ds_read_b64_tr_b16 v[114:115], v130 offset:2048
	ds_read_b64_tr_b16 v[108:109], v2 offset:4096
	ds_read_b64_tr_b16 v[110:111], v128 offset:4096
	ds_read_b64_tr_b16 v[104:105], v129 offset:4096
	ds_read_b64_tr_b16 v[106:107], v130 offset:4096
	ds_read_b64_tr_b16 v[100:101], v2 offset:6144
	ds_read_b64_tr_b16 v[102:103], v128 offset:6144
	ds_read_b64_tr_b16 v[96:97], v129 offset:6144
	ds_read_b64_tr_b16 v[98:99], v130 offset:6144
	s_waitcnt lgkmcnt(0)
	v_mfma_f32_16x16x32_bf16 v[184:187], v[184:187], v[202:205], v[132:135]
	v_mfma_f32_16x16x32_bf16 v[16:19], v[124:127], v[68:71], v[16:19]
	v_mfma_f32_16x16x32_bf16 v[12:15], v[120:123], v[68:71], v[12:15]
	v_mfma_f32_16x16x32_bf16 v[16:19], v[116:119], v[72:75], v[16:19]
	v_mfma_f32_16x16x32_bf16 v[12:15], v[112:115], v[72:75], v[12:15]
	v_mfma_f32_16x16x32_bf16 v[16:19], v[108:111], v[76:79], v[16:19]
	v_mfma_f32_16x16x32_bf16 v[12:15], v[104:107], v[76:79], v[12:15]
	v_mfma_f32_16x16x32_bf16 v[188:191], v[188:191], v[202:205], v[136:139]
	v_mfma_f32_16x16x32_bf16 v[192:195], v[192:195], v[202:205], v[140:143]
	v_mfma_f32_16x16x32_bf16 v[196:199], v[196:199], v[202:205], v[144:147]
	v_mfma_f32_16x16x32_bf16 v[16:19], v[100:103], v[80:83], v[16:19]
	v_mfma_f32_16x16x32_bf16 v[12:15], v[96:99], v[80:83], v[12:15]
	s_cbranch_vccnz .LBB0_65
	s_waitcnt vmcnt(14)
	s_cbranch_execnz .LBB0_52

; template <int VAR  >
; __device__ __forceinline__ void ret_core_mfma(const bf16* P, const bf16* VT, const float* decay_logit  , bf16* YF, bf16* YB, float* PT, LAS unsigned char* lds, const int tid, const int bid, const int G) {
;     ...
;             for (int ks = 0; ks < 8; ++ks) {
;                 if (ks < 4) { if (c == 0) RC_WAITV(6); else RC_WAITV(14); } else if (ks == 4) RC_WAITV(6); else if (ks == 5) RC_WAITV(5); else if (ks == 6) RC_WAITV(4); else RC_WAITV(3);
;                 RC_BAR();
;                 { const int s4 = RC_PREV(slot);
;                   if (ks + 4 < 12) RC_ISSUE(ks + 4, tok0, s4); else RC_ISSUE(ks + 4 - 12, tokn, s4); }
;                 bf16x8v At[4], Bk[2], Bs[2];
;                 const LAS unsigned char* sq = lds + RC_RG + slot * 16384;
; #pragma unroll
;                 for (int m = 0; m < 4; ++m) At[m] = *(const LAS bf16x8v*)(sq + aoff + m * 1024);
; #pragma unroll
;                 for (int n = 0; n < 2; ++n) { Bk[n] = *(const LAS bf16x8v*)(sq + 8192 + boff + n * 1024); Bs[n] = *(const LAS bf16x8v*)(lds + RC_ST + ks * 8192 + boff + n * 1024); }
; #pragma unroll
;                 for (int m = 0; m < 4; ++m)
; #pragma unroll
;                     for (int n = 0; n < 2; ++n) { accA[m][n] = RC_MFMA(Bk[n], At[m], accA[m][n]); accY[m][n] = RC_MFMA(Bs[n], At[m], accY[m][n]); }
;                 { const unsigned kb = (unsigned)(size_t)(sq + 8192);
;                   const unsigned a0 = kb + trA, a1 = kb + trB, b0 = kb + (trA ^ 32u), b1 = kb + (trB ^ 32u);
;                   v2u l0, h0, l1, h1, l2, h2, l3, h3, p0, q0, p1, q1, p2, q2, p3, q3;
;                   asm volatile("ds_read_b64_tr_b16 %0, %16\n\tds_read_b64_tr_b16 %1, %17\n\tds_read_b64_tr_b16 %8, %18\n\tds_read_b64_tr_b16 %9, %19\n\t"
;                                "ds_read_b64_tr_b16 %2, %16 offset:2048\n\tds_read_b64_tr_b16 %3, %17 offset:2048\n\tds_read_b64_tr_b16 %10, %18 offset:2048\n\tds_read_b64_tr_b16 %11, %19 offset:2048\n\t"
;                                "ds_read_b64_tr_b16 %4, %16 offset:4096\n\tds_read_b64_tr_b16 %5, %17 offset:4096\n\tds_read_b64_tr_b16 %12, %18 offset:4096\n\tds_read_b64_tr_b16 %13, %19 offset:4096\n\t"
;                                "ds_read_b64_tr_b16 %6, %16 offset:6144\n\tds_read_b64_tr_b16 %7, %17 offset:6144\n\tds_read_b64_tr_b16 %14, %18 offset:6144\n\tds_read_b64_tr_b16 %15, %19 offset:6144\n\ts_waitcnt lgkmcnt(0)"
.LBB0_52:
	s_add_i32 s0, s40, 1
	s_cmp_lg_u32 s40, 4
	s_cselect_b32 s40, s0, 0
	s_mov_b64 s[0:1], 0x180
	s_lshl_b32 s41, s40, 14
	v_lshl_add_u64 v[96:97], v[232:233], 0, s[0:1]
	s_add_i32 s0, s41, 0xffffc000
	s_cmp_lg_u32 s40, 0
	s_cselect_b32 s0, s0, 0x10000
	s_add_i32 s0, s0, 0
	s_add_i32 s42, s0, s44
	s_barrier
	s_add_i32 s0, s41, 0
	s_add_i32 s1, s0, 0x10000
	v_add_u32_e32 v2, s1, v242
	ds_read_b128 v[202:205], v236 offset:17408
	ds_read_b128 v[208:211], v236 offset:16384
	ds_read_b128 v[108:111], v2
	ds_read_b128 v[124:127], v2 offset:1024
	ds_read_b128 v[140:143], v2 offset:2048
	ds_read_b128 v[246:249], v2 offset:3072
	v_add_u32_e32 v2, s1, v243
	ds_read_b128 v[144:147], v2 offset:8192
	ds_read_b128 v[238:241], v2 offset:9216
	s_add_i32 m0, s42, 0x10000
	s_mov_b64 s[98:99], 0x980
	global_load_lds_dwordx4 v[96:97], off
	v_lshl_add_u64 v[96:97], v[232:233], 0, s[98:99]
	s_add_i32 m0, s42, 0x12000
	s_nop 0
	global_load_lds_dwordx4 v[96:97], off
	v_mov_b32_e32 v217, v216
	v_pk_mul_f32 v[10:11], v[216:217], v[10:11]
	v_pk_mul_f32 v[8:9], v[224:225], v[8:9]
	v_pk_mul_f32 v[6:7], v[216:217], v[6:7]
	v_pk_mul_f32 v[4:5], v[224:225], v[4:5]
	s_add_i32 s0, s0, 0x12000
	s_waitcnt lgkmcnt(0)
	v_mfma_f32_16x16x32_bf16 v[96:99], v[144:147], v[108:111], v[84:87]
	v_add_u32_e32 v2, s0, v234
	s_and_b64 vcc, exec, s[6:7]
	v_mfma_f32_16x16x32_bf16 v[100:103], v[208:211], v[108:111], v[88:91]
	v_mfma_f32_16x16x32_bf16 v[104:107], v[238:241], v[108:111], v[92:95]
	v_mfma_f32_16x16x32_bf16 v[108:111], v[202:205], v[108:111], v[148:151]
	v_mfma_f32_16x16x32_bf16 v[112:115], v[144:147], v[124:127], v[152:155]
	v_mfma_f32_16x16x32_bf16 v[116:119], v[208:211], v[124:127], v[156:159]
	v_mfma_f32_16x16x32_bf16 v[120:123], v[238:241], v[124:127], v[160:163]
	v_mfma_f32_16x16x32_bf16 v[124:127], v[202:205], v[124:127], v[164:167]
	v_mfma_f32_16x16x32_bf16 v[128:131], v[144:147], v[140:143], v[168:171]
	v_mfma_f32_16x16x32_bf16 v[132:135], v[208:211], v[140:143], v[172:175]
	v_mfma_f32_16x16x32_bf16 v[136:139], v[238:241], v[140:143], v[176:179]
	v_mfma_f32_16x16x32_bf16 v[140:143], v[202:205], v[140:143], v[180:183]
	s_nop 2
	v_add_u32_e32 v180, s0, v231
	v_add_u32_e32 v181, s0, v227
	v_add_u32_e32 v182, s0, v229
	ds_read_b64_tr_b16 v[176:177], v2
	ds_read_b64_tr_b16 v[178:179], v180
	ds_read_b64_tr_b16 v[172:173], v181
	ds_read_b64_tr_b16 v[174:175], v182
	ds_read_b64_tr_b16 v[168:169], v2 offset:2048
	ds_read_b64_tr_b16 v[170:171], v180 offset:2048
	ds_read_b64_tr_b16 v[164:165], v181 offset:2048
	ds_read_b64_tr_b16 v[166:167], v182 offset:2048
	ds_read_b64_tr_b16 v[160:161], v2 offset:4096
	ds_read_b64_tr_b16 v[162:163], v180 offset:4096
	ds_read_b64_tr_b16 v[156:157], v181 offset:4096
	ds_read_b64_tr_b16 v[158:159], v182 offset:4096
	ds_read_b64_tr_b16 v[152:153], v2 offset:6144
	ds_read_b64_tr_b16 v[154:155], v180 offset:6144
	ds_read_b64_tr_b16 v[148:149], v181 offset:6144
	ds_read_b64_tr_b16 v[150:151], v182 offset:6144
	s_waitcnt lgkmcnt(0)
	v_mfma_f32_16x16x32_bf16 v[144:147], v[144:147], v[246:249], v[184:187]
	v_mfma_f32_16x16x32_bf16 v[8:11], v[176:179], v[68:71], v[8:11]
	v_mfma_f32_16x16x32_bf16 v[4:7], v[172:175], v[68:71], v[4:7]
	v_mfma_f32_16x16x32_bf16 v[8:11], v[168:171], v[72:75], v[8:11]
	v_mfma_f32_16x16x32_bf16 v[4:7], v[164:167], v[72:75], v[4:7]
	v_mfma_f32_16x16x32_bf16 v[8:11], v[160:163], v[76:79], v[8:11]
	v_mfma_f32_16x16x32_bf16 v[4:7], v[156:159], v[76:79], v[4:7]
	v_mfma_f32_16x16x32_bf16 v[88:91], v[208:211], v[246:249], v[188:191]
	v_mfma_f32_16x16x32_bf16 v[84:87], v[238:241], v[246:249], v[192:195]
	v_mfma_f32_16x16x32_bf16 v[92:95], v[202:205], v[246:249], v[196:199]
	v_mfma_f32_16x16x32_bf16 v[8:11], v[152:155], v[80:83], v[8:11]
	v_mfma_f32_16x16x32_bf16 v[4:7], v[148:151], v[80:83], v[4:7]
	s_cbranch_vccnz .LBB0_66
	s_waitcnt vmcnt(14)
	s_cbranch_execnz .LBB0_55

; #define LAS __attribute__((address_space(3)))
; template <int VAR  >
; __device__ __forceinline__ void ret_core_mfma(const bf16* P, const bf16* VT, const float* decay_logit  , bf16* YF, bf16* YB, float* PT, LAS unsigned char* lds, const int tid, const int bid, const int G) {
;     ...
;             for (int n = 0; n < 16; ++n) acc4[n] = acc4[n] * cdec;
;             const int jj = 8 * fqc + (frc >> 2);
;             const unsigned trA = (unsigned)((jj >> 4) * 1024 + sl_swz((jj & 15) * 64 + 8 * (frc & 3))), trB = (unsigned)(((jj + 4) >> 4) * 1024 + sl_swz(((jj + 4) & 15) * 64 + 8 * (frc & 3)));
;             f32x4 accA[4][2], accY[4][2];
; #pragma unroll
;             for (int m = 0; m < 4; ++m)
; #pragma unroll
;                 for (int n = 0; n < 2; ++n) { accA[m][n] = (f32x4){0.f, 0.f, 0.f, 0.f}; accY[m][n] = (f32x4){0.f, 0.f, 0.f, 0.f}; }
; #pragma unroll
;             for (int ks = 0; ks < 8; ++ks) {
;                 if (ks < 4) { if (c == 0) RC_WAITV(6); else RC_WAITV(14); } else if (ks == 4) RC_WAITV(6); else if (ks == 5) RC_WAITV(5); else if (ks == 6) RC_WAITV(4); else RC_WAITV(3);
;                 RC_BAR();
;                 { const int s4 = RC_PREV(slot);
;                   if (ks + 4 < 12) RC_ISSUE(ks + 4, tok0, s4); else RC_ISSUE(ks + 4 - 12, tokn, s4); }
;                 bf16x8v At[4], Bk[2], Bs[2];
;                 const LAS unsigned char* sq = lds + RC_RG + slot * 16384;
; #pragma unroll
;                 for (int m = 0; m < 4; ++m) At[m] = *(const LAS bf16x8v*)(sq + aoff + m * 1024);
; #pragma unroll
;                 for (int n = 0; n < 2; ++n) { Bk[n] = *(const LAS bf16x8v*)(sq + 8192 + boff + n * 1024); Bs[n] = *(const LAS bf16x8v*)(lds + RC_ST + ks * 8192 + boff + n * 1024); }
; #pragma unroll
;                 for (int m = 0; m < 4; ++m)
; #pragma unroll
;                     for (int n = 0; n < 2; ++n) { accA[m][n] = RC_MFMA(Bk[n], At[m], accA[m][n]); accY[m][n] = RC_MFMA(Bs[n], At[m], accY[m][n]); }
;                 { const unsigned kb = (unsigned)(size_t)(sq + 8192);
;                   const unsigned a0 = kb + trA, a1 = kb + trB, b0 = kb + (trA ^ 32u), b1 = kb + (trB ^ 32u);
;                   v2u l0, h0, l1, h1, l2, h2, l3, h3, p0, q0, p1, q1, p2, q2, p3, q3;
;                   asm volatile("ds_read_b64_tr_b16 %0, %16\n\tds_read_b64_tr_b16 %1, %17\n\tds_read_b64_tr_b16 %8, %18\n\tds_read_b64_tr_b16 %9, %19\n\t"
.LBB0_55:
	s_add_i32 s0, s40, 1
	s_cmp_lg_u32 s40, 4
	s_cselect_b32 s0, s0, 0
	s_lshl_b32 s60, s38, 7
	s_add_i32 s6, s33, 1
	s_cmp_eq_u32 s33, 15
	s_cselect_b32 s1, 0, s39
	s_cselect_b32 s7, 15, s6
	s_and_b64 s[40:41], s[4:5], exec
	s_cselect_b32 s7, s7, s1
	s_lshl_b32 s1, s0, 14
	s_lshl_b32 s40, s38, 8
	s_add_i32 s33, s1, 0xffffc000
	s_cmp_lg_u32 s0, 0
	s_cselect_b32 s33, s33, 0x10000
	s_mov_b32 s41, s61
	s_add_i32 s33, s33, 0
	v_lshl_add_u64 v[148:149], v[220:221], 0, s[40:41]
	s_mov_b64 s[40:41], 0x1c0
	s_add_i32 s33, s33, s44
	s_barrier
	s_add_i32 s1, s86, s1
	v_add_u32_e32 v170, s1, v242
	v_add_u32_e32 v178, s1, v243
	ds_read_b128 v[150:153], v236 offset:25600
	ds_read_b128 v[154:157], v236 offset:24576
	ds_read_b128 v[158:161], v170
	ds_read_b128 v[162:165], v170 offset:1024
	ds_read_b128 v[166:169], v170 offset:2048
	ds_read_b128 v[170:173], v170 offset:3072
	ds_read_b128 v[174:177], v178 offset:8192
	ds_read_b128 v[178:181], v178 offset:9216
	v_lshl_add_u64 v[182:183], v[232:233], 0, s[40:41]
	s_add_i32 m0, s33, 0x10000
	s_mov_b64 s[98:99], 0x9c0
	global_load_lds_dwordx4 v[182:183], off
	v_lshl_add_u64 v[182:183], v[232:233], 0, s[98:99]
	s_add_i32 m0, s33, 0x12000
	s_nop 0
	global_load_lds_dwordx4 v[182:183], off
	v_mov_b32_e32 v217, v216
	v_pk_mul_f32 v[26:27], v[216:217], v[26:27]
	v_pk_mul_f32 v[24:25], v[224:225], v[24:25]
	v_pk_mul_f32 v[22:23], v[216:217], v[22:23]
	v_pk_mul_f32 v[20:21], v[224:225], v[20:21]
	s_add_i32 s33, s1, 0x2000
	s_waitcnt lgkmcnt(0)
	v_mfma_f32_16x16x32_bf16 v[96:99], v[174:177], v[158:161], v[96:99]
	v_add_u32_e32 v182, s33, v234
	v_add_u32_e32 v183, s33, v231
	v_add_u32_e32 v184, s33, v227
	v_mfma_f32_16x16x32_bf16 v[100:103], v[154:157], v[158:161], v[100:103]
	v_add_u32_e32 v185, s33, v229
	s_add_i32 s1, s0, 1
	s_cmp_lg_u32 s0, 4
	v_mfma_f32_16x16x32_bf16 v[104:107], v[178:181], v[158:161], v[104:107]
	s_cselect_b32 s0, s1, 0
	s_lshl_b32 s1, s0, 14
	s_add_i32 s33, s1, 0xffffc000
	v_mfma_f32_16x16x32_bf16 v[108:111], v[150:153], v[158:161], v[108:111]
	s_cmp_lg_u32 s0, 0
	s_cselect_b32 s33, s33, 0x10000
	s_add_i32 s33, s33, 0
	v_mfma_f32_16x16x32_bf16 v[112:115], v[174:177], v[162:165], v[112:115]
	s_add_i32 s33, s33, s44
	s_add_i32 m0, s33, 0x10000
	s_add_i32 s1, s86, s1
	v_mfma_f32_16x16x32_bf16 v[116:119], v[154:157], v[162:165], v[116:119]
	v_mul_f32_e64 v30, v216, v30
	v_mul_f32_e64 v31, v217, v31
	v_pk_mul_f32 v[28:29], v[224:225], v[28:29]
	s_add_i32 s33, s1, 0x2000
	v_mfma_f32_16x16x32_bf16 v[120:123], v[178:181], v[162:165], v[120:123]
	v_mul_f32_e64 v34, v216, v34
	v_mul_f32_e64 v35, v217, v35
	v_pk_mul_f32 v[32:33], v[224:225], v[32:33]
	v_pk_mul_f32 v[46:47], v[216:217], v[46:47]
	v_mfma_f32_16x16x32_bf16 v[124:127], v[150:153], v[162:165], v[124:127]
	v_mul_f32_e64 v44, v224, v44
	v_mul_f32_e64 v45, v225, v45
	v_pk_mul_f32 v[50:51], v[216:217], v[50:51]
	v_pk_mul_f32 v[48:49], v[224:225], v[48:49]
	v_mfma_f32_16x16x32_bf16 v[128:131], v[174:177], v[166:169], v[128:131]
	v_mul_f32_e64 v58, v216, v58
	v_mul_f32_e64 v59, v217, v59
	v_pk_mul_f32 v[56:57], v[224:225], v[56:57]
	v_pk_mul_f32 v[54:55], v[216:217], v[54:55]
	v_mfma_f32_16x16x32_bf16 v[132:135], v[154:157], v[166:169], v[132:135]
	v_mul_f32_e64 v52, v224, v52
	v_mul_f32_e64 v53, v225, v53
	v_pk_mul_f32 v[62:63], v[216:217], v[62:63]
	v_pk_mul_f32 v[60:61], v[224:225], v[60:61]
	v_mfma_f32_16x16x32_bf16 v[136:139], v[178:181], v[166:169], v[136:139]
	v_mul_f32_e64 v66, v216, v66
	v_mul_f32_e64 v67, v217, v67
	v_pk_mul_f32 v[64:65], v[224:225], v[64:65]
	v_and_b32_e32 v2, 15, v230
	v_mfma_f32_16x16x32_bf16 v[140:143], v[150:153], v[166:169], v[140:143]
	v_mfma_f32_16x16x32_bf16 v[144:147], v[174:177], v[170:173], v[144:147]
	v_mfma_f32_16x16x32_bf16 v[88:91], v[154:157], v[170:173], v[88:91]
	v_mfma_f32_16x16x32_bf16 v[84:87], v[178:181], v[170:173], v[84:87]
	v_mfma_f32_16x16x32_bf16 v[92:95], v[150:153], v[170:173], v[92:95]
	ds_read_b64_tr_b16 v[178:179], v182
	ds_read_b64_tr_b16 v[180:181], v183
	ds_read_b64_tr_b16 v[174:175], v184
	ds_read_b64_tr_b16 v[176:177], v185
	ds_read_b64_tr_b16 v[170:171], v182 offset:2048
	ds_read_b64_tr_b16 v[172:173], v183 offset:2048
	ds_read_b64_tr_b16 v[166:167], v184 offset:2048
	ds_read_b64_tr_b16 v[168:169], v185 offset:2048
	ds_read_b64_tr_b16 v[162:163], v182 offset:4096
	ds_read_b64_tr_b16 v[164:165], v183 offset:4096
	ds_read_b64_tr_b16 v[158:159], v184 offset:4096
	ds_read_b64_tr_b16 v[160:161], v185 offset:4096
	ds_read_b64_tr_b16 v[154:155], v182 offset:6144
	ds_read_b64_tr_b16 v[156:157], v183 offset:6144
	ds_read_b64_tr_b16 v[150:151], v184 offset:6144
	ds_read_b64_tr_b16 v[152:153], v185 offset:6144
	s_waitcnt lgkmcnt(0)
	s_waitcnt vmcnt(6)
	s_barrier
; template <int VAR  >
; __device__ __forceinline__ void ret_core_mfma(const bf16* P, const bf16* VT, const float* decay_logit  , bf16* YF, bf16* YB, float* PT, LAS unsigned char* lds, const int tid, const int bid, const int G) {
;     ...
;             for (int ks = 0; ks < 8; ++ks) {
;                 if (ks < 4) { if (c == 0) RC_WAITV(6); else RC_WAITV(14); } else if (ks == 4) RC_WAITV(6); else if (ks == 5) RC_WAITV(5); else if (ks == 6) RC_WAITV(4); else RC_WAITV(3);
;                 RC_BAR();
;                 { const int s4 = RC_PREV(slot);
;                   if (ks + 4 < 12) RC_ISSUE(ks + 4, tok0, s4); else RC_ISSUE(ks + 4 - 12, tokn, s4); }
;                 bf16x8v At[4], Bk[2], Bs[2];
;                 const LAS unsigned char* sq = lds + RC_RG + slot * 16384;
; #pragma unroll
;                 for (int m = 0; m < 4; ++m) At[m] = *(const LAS bf16x8v*)(sq + aoff + m * 1024);
; #pragma unroll
;                 for (int n = 0; n < 2; ++n) { Bk[n] = *(const LAS bf16x8v*)(sq + 8192 + boff + n * 1024); Bs[n] = *(const LAS bf16x8v*)(lds + RC_ST + ks * 8192 + boff + n * 1024); }
; #pragma unroll
;                 for (int m = 0; m < 4; ++m)
; #pragma unroll
;                     for (int n = 0; n < 2; ++n) { accA[m][n] = RC_MFMA(Bk[n], At[m], accA[m][n]); accY[m][n] = RC_MFMA(Bs[n], At[m], accY[m][n]); }
;                 { const unsigned kb = (unsigned)(size_t)(sq + 8192);
;                   const unsigned a0 = kb + trA, a1 = kb + trB, b0 = kb + (trA ^ 32u), b1 = kb + (trB ^ 32u);
;                   v2u l0, h0, l1, h1, l2, h2, l3, h3, p0, q0, p1, q1, p2, q2, p3, q3;
;                   asm volatile("ds_read_b64_tr_b16 %0, %16\n\tds_read_b64_tr_b16 %1, %17\n\tds_read_b64_tr_b16 %8, %18\n\tds_read_b64_tr_b16 %9, %19\n\t"
;                                "ds_read_b64_tr_b16 %2, %16 offset:2048\n\tds_read_b64_tr_b16 %3, %17 offset:2048\n\tds_read_b64_tr_b16 %10, %18 offset:2048\n\tds_read_b64_tr_b16 %11, %19 offset:2048\n\t"
;                                "ds_read_b64_tr_b16 %4, %16 offset:4096\n\tds_read_b64_tr_b16 %5, %17 offset:4096\n\tds_read_b64_tr_b16 %12, %18 offset:4096\n\tds_read_b64_tr_b16 %13, %19 offset:4096\n\t"
;                                "ds_read_b64_tr_b16 %6, %16 offset:6144\n\tds_read_b64_tr_b16 %7, %17 offset:6144\n\tds_read_b64_tr_b16 %14, %18 offset:6144\n\tds_read_b64_tr_b16 %15, %19 offset:6144\n\ts_waitcnt lgkmcnt(0)"
	v_mfma_f32_16x16x32_bf16 v[24:27], v[178:181], v[68:71], v[24:27]
	global_load_lds_dwordx4 v[148:149], off
	v_mfma_f32_16x16x32_bf16 v[20:23], v[174:177], v[68:71], v[20:23]
	v_add_u32_e32 v178, s1, v243
	v_mfma_f32_16x16x32_bf16 v[24:27], v[170:173], v[72:75], v[24:27]
	v_add_u32_e32 v170, s1, v242
	s_add_i32 s1, s0, 1
	s_cmp_lg_u32 s0, 4
	v_mfma_f32_16x16x32_bf16 v[20:23], v[166:169], v[72:75], v[20:23]
	s_cselect_b32 s0, s1, 0
	s_lshl_b32 s1, s0, 14
	v_mfma_f32_16x16x32_bf16 v[24:27], v[162:165], v[76:79], v[24:27]
	v_mfma_f32_16x16x32_bf16 v[20:23], v[158:161], v[76:79], v[20:23]
	v_mfma_f32_16x16x32_bf16 v[24:27], v[154:157], v[80:83], v[24:27]
	v_mfma_f32_16x16x32_bf16 v[20:23], v[150:153], v[80:83], v[20:23]
	ds_read_b128 v[150:153], v236 offset:33792
	ds_read_b128 v[154:157], v236 offset:32768
	ds_read_b128 v[158:161], v170
	ds_read_b128 v[162:165], v170 offset:1024
	ds_read_b128 v[166:169], v170 offset:2048
	ds_read_b128 v[170:173], v170 offset:3072
	ds_read_b128 v[174:177], v178 offset:8192
	ds_read_b128 v[178:181], v178 offset:9216
	s_waitcnt lgkmcnt(0)
	v_mfma_f32_16x16x32_bf16 v[96:99], v[174:177], v[158:161], v[96:99]
	v_mfma_f32_16x16x32_bf16 v[100:103], v[154:157], v[158:161], v[100:103]
	v_mfma_f32_16x16x32_bf16 v[104:107], v[178:181], v[158:161], v[104:107]
	v_mfma_f32_16x16x32_bf16 v[108:111], v[150:153], v[158:161], v[108:111]
	v_mfma_f32_16x16x32_bf16 v[112:115], v[174:177], v[162:165], v[112:115]
	v_mfma_f32_16x16x32_bf16 v[158:161], v[154:157], v[162:165], v[116:119]
	v_mfma_f32_16x16x32_bf16 v[182:185], v[178:181], v[162:165], v[120:123]
	v_mfma_f32_16x16x32_bf16 v[162:165], v[150:153], v[162:165], v[124:127]
	v_mfma_f32_16x16x32_bf16 v[186:189], v[174:177], v[166:169], v[128:131]
	v_mfma_f32_16x16x32_bf16 v[132:135], v[154:157], v[166:169], v[132:135]
	v_mfma_f32_16x16x32_bf16 v[120:123], v[178:181], v[166:169], v[136:139]
	v_mfma_f32_16x16x32_bf16 v[124:127], v[150:153], v[166:169], v[140:143]
	v_mfma_f32_16x16x32_bf16 v[128:131], v[174:177], v[170:173], v[144:147]
	v_add_u32_e32 v174, s33, v234
	v_add_u32_e32 v175, s33, v231
	v_add_u32_e32 v176, s33, v227
	v_mfma_f32_16x16x32_bf16 v[136:139], v[154:157], v[170:173], v[88:91]
	v_add_u32_e32 v177, s33, v229
	s_add_i32 s33, s1, 0xffffc000
	s_cmp_lg_u32 s0, 0
	v_mfma_f32_16x16x32_bf16 v[140:143], v[178:181], v[170:173], v[84:87]
	s_cselect_b32 s33, s33, 0x10000
	s_add_i32 s33, s33, 0
	s_add_i32 s33, s33, s44
	v_mfma_f32_16x16x32_bf16 v[150:153], v[150:153], v[170:173], v[92:95]
	ds_read_b64_tr_b16 v[170:171], v174
	ds_read_b64_tr_b16 v[172:173], v175
	ds_read_b64_tr_b16 v[166:167], v176
	ds_read_b64_tr_b16 v[168:169], v177
	ds_read_b64_tr_b16 v[154:155], v174 offset:2048
	ds_read_b64_tr_b16 v[156:157], v175 offset:2048
	ds_read_b64_tr_b16 v[144:145], v176 offset:2048
	ds_read_b64_tr_b16 v[146:147], v177 offset:2048
	ds_read_b64_tr_b16 v[116:117], v174 offset:4096
	ds_read_b64_tr_b16 v[118:119], v175 offset:4096
	ds_read_b64_tr_b16 v[92:93], v176 offset:4096
	ds_read_b64_tr_b16 v[94:95], v177 offset:4096
	ds_read_b64_tr_b16 v[88:89], v174 offset:6144
	ds_read_b64_tr_b16 v[90:91], v175 offset:6144
	ds_read_b64_tr_b16 v[84:85], v176 offset:6144
	ds_read_b64_tr_b16 v[86:87], v177 offset:6144
	s_waitcnt lgkmcnt(0)
	s_waitcnt vmcnt(5)
	s_barrier
	v_mfma_f32_16x16x32_bf16 v[28:31], v[166:169], v[68:71], v[28:31]
	s_add_i32 m0, s33, 0x10000
	s_add_i32 s1, s86, s1
	v_mfma_f32_16x16x32_bf16 v[32:35], v[170:173], v[68:71], v[32:35]
	s_add_i32 s33, s1, 0x2000
	v_mfma_f32_16x16x32_bf16 v[28:31], v[144:147], v[72:75], v[28:31]
	v_mfma_f32_16x16x32_bf16 v[32:35], v[154:157], v[72:75], v[32:35]
	v_mfma_f32_16x16x32_bf16 v[28:31], v[92:95], v[76:79], v[28:31]
	v_mfma_f32_16x16x32_bf16 v[32:35], v[116:119], v[76:79], v[32:35]
	v_mfma_f32_16x16x32_bf16 v[28:31], v[84:87], v[80:83], v[28:31]
	v_lshl_add_u64 v[84:85], v[148:149], 0, 64
	global_load_lds_dwordx4 v[84:85], off
	v_mfma_f32_16x16x32_bf16 v[32:35], v[88:91], v[80:83], v[32:35]
	v_add_u32_e32 v88, s1, v242
	ds_read_b128 v[154:157], v236 offset:41984
	ds_read_b128 v[166:169], v236 offset:40960
	ds_read_b128 v[84:87], v88
	ds_read_b128 v[170:173], v88 offset:1024
	ds_read_b128 v[174:177], v88 offset:2048
	ds_read_b128 v[178:181], v88 offset:3072
	v_add_u32_e32 v88, s1, v243
	ds_read_b128 v[190:193], v88 offset:8192
	ds_read_b128 v[194:197], v88 offset:9216
	s_waitcnt lgkmcnt(0)
	v_mfma_f32_16x16x32_bf16 v[144:147], v[190:193], v[84:87], v[96:99]
	s_add_i32 s1, s0, 1
	s_cmp_lg_u32 s0, 4
	s_cselect_b32 s0, s1, 0
	v_mfma_f32_16x16x32_bf16 v[116:119], v[166:169], v[84:87], v[100:103]
	s_lshl_b32 s1, s0, 14
	v_mfma_f32_16x16x32_bf16 v[104:107], v[194:197], v[84:87], v[104:107]
	v_mfma_f32_16x16x32_bf16 v[84:87], v[154:157], v[84:87], v[108:111]
	v_mfma_f32_16x16x32_bf16 v[88:91], v[190:193], v[170:173], v[112:115]
	v_mfma_f32_16x16x32_bf16 v[92:95], v[166:169], v[170:173], v[158:161]
	v_mfma_f32_16x16x32_bf16 v[96:99], v[194:197], v[170:173], v[182:185]
	v_mfma_f32_16x16x32_bf16 v[100:103], v[154:157], v[170:173], v[162:165]
	s_nop 1
	v_add_u32_e32 v182, s33, v234
	v_add_u32_e32 v183, s33, v231
	v_add_u32_e32 v184, s33, v227
	v_mfma_f32_16x16x32_bf16 v[108:111], v[190:193], v[174:177], v[186:189]
	v_add_u32_e32 v185, s33, v229
	s_add_i32 s33, s1, 0xffffc000
	s_cmp_lg_u32 s0, 0
	v_mfma_f32_16x16x32_bf16 v[112:115], v[166:169], v[174:177], v[132:135]
	s_cselect_b32 s33, s33, 0x10000
	s_add_i32 s33, s33, 0
	s_add_i32 s33, s33, s44
	v_mfma_f32_16x16x32_bf16 v[120:123], v[194:197], v[174:177], v[120:123]
	s_add_i32 m0, s33, 0x10000
	s_add_i32 s1, s86, s1
	s_add_i32 s33, s1, 0x2000
	v_mfma_f32_16x16x32_bf16 v[124:127], v[154:157], v[174:177], v[124:127]
	v_mfma_f32_16x16x32_bf16 v[128:131], v[190:193], v[178:181], v[128:131]
	v_mfma_f32_16x16x32_bf16 v[132:135], v[166:169], v[178:181], v[136:139]
	v_mfma_f32_16x16x32_bf16 v[136:139], v[194:197], v[178:181], v[140:143]
	v_mfma_f32_16x16x32_bf16 v[140:143], v[154:157], v[178:181], v[150:153]
	ds_read_b64_tr_b16 v[178:179], v182
	ds_read_b64_tr_b16 v[180:181], v183
	ds_read_b64_tr_b16 v[174:175], v184
	ds_read_b64_tr_b16 v[176:177], v185
	ds_read_b64_tr_b16 v[170:171], v182 offset:2048
	ds_read_b64_tr_b16 v[172:173], v183 offset:2048
	ds_read_b64_tr_b16 v[166:167], v184 offset:2048
	ds_read_b64_tr_b16 v[168:169], v185 offset:2048
	ds_read_b64_tr_b16 v[162:163], v182 offset:4096
	ds_read_b64_tr_b16 v[164:165], v183 offset:4096
	ds_read_b64_tr_b16 v[158:159], v184 offset:4096
	ds_read_b64_tr_b16 v[160:161], v185 offset:4096
	ds_read_b64_tr_b16 v[154:155], v182 offset:6144
	ds_read_b64_tr_b16 v[156:157], v183 offset:6144
	ds_read_b64_tr_b16 v[150:151], v184 offset:6144
	ds_read_b64_tr_b16 v[152:153], v185 offset:6144
	s_waitcnt lgkmcnt(0)
	s_waitcnt vmcnt(4)
	s_barrier
; template <int VAR  >
; __device__ __forceinline__ void ret_core_mfma(const bf16* P, const bf16* VT, const float* decay_logit  , bf16* YF, bf16* YB, float* PT, LAS unsigned char* lds, const int tid, const int bid, const int G) {
;     ...
;             for (int ks = 0; ks < 8; ++ks) {
;                 if (ks < 4) { if (c == 0) RC_WAITV(6); else RC_WAITV(14); } else if (ks == 4) RC_WAITV(6); else if (ks == 5) RC_WAITV(5); else if (ks == 6) RC_WAITV(4); else RC_WAITV(3);
;                 RC_BAR();
;                 { const int s4 = RC_PREV(slot);
;                   if (ks + 4 < 12) RC_ISSUE(ks + 4, tok0, s4); else RC_ISSUE(ks + 4 - 12, tokn, s4); }
;                 bf16x8v At[4], Bk[2], Bs[2];
;                 const LAS unsigned char* sq = lds + RC_RG + slot * 16384;
; #pragma unroll
;                 for (int m = 0; m < 4; ++m) At[m] = *(const LAS bf16x8v*)(sq + aoff + m * 1024);
; #pragma unroll
;                 for (int n = 0; n < 2; ++n) { Bk[n] = *(const LAS bf16x8v*)(sq + 8192 + boff + n * 1024); Bs[n] = *(const LAS bf16x8v*)(lds + RC_ST + ks * 8192 + boff + n * 1024); }
; #pragma unroll
;                 for (int m = 0; m < 4; ++m)
; #pragma unroll
;                     for (int n = 0; n < 2; ++n) { accA[m][n] = RC_MFMA(Bk[n], At[m], accA[m][n]); accY[m][n] = RC_MFMA(Bs[n], At[m], accY[m][n]); }
;                 { const unsigned kb = (unsigned)(size_t)(sq + 8192);
;                   const unsigned a0 = kb + trA, a1 = kb + trB, b0 = kb + (trA ^ 32u), b1 = kb + (trB ^ 32u);
;                   v2u l0, h0, l1, h1, l2, h2, l3, h3, p0, q0, p1, q1, p2, q2, p3, q3;
;                   asm volatile("ds_read_b64_tr_b16 %0, %16\n\tds_read_b64_tr_b16 %1, %17\n\tds_read_b64_tr_b16 %8, %18\n\tds_read_b64_tr_b16 %9, %19\n\t"
;                                "ds_read_b64_tr_b16 %2, %16 offset:2048\n\tds_read_b64_tr_b16 %3, %17 offset:2048\n\tds_read_b64_tr_b16 %10, %18 offset:2048\n\tds_read_b64_tr_b16 %11, %19 offset:2048\n\t"
;                                "ds_read_b64_tr_b16 %4, %16 offset:4096\n\tds_read_b64_tr_b16 %5, %17 offset:4096\n\tds_read_b64_tr_b16 %12, %18 offset:4096\n\tds_read_b64_tr_b16 %13, %19 offset:4096\n\t"
;                                "ds_read_b64_tr_b16 %6, %16 offset:6144\n\tds_read_b64_tr_b16 %7, %17 offset:6144\n\tds_read_b64_tr_b16 %14, %18 offset:6144\n\tds_read_b64_tr_b16 %15, %19 offset:6144\n\ts_waitcnt lgkmcnt(0)"
	v_mfma_f32_16x16x32_bf16 v[44:47], v[174:177], v[68:71], v[44:47]
	v_mfma_f32_16x16x32_bf16 v[48:51], v[178:181], v[68:71], v[48:51]
	v_add_u32_e32 v178, s1, v243
	v_mfma_f32_16x16x32_bf16 v[44:47], v[166:169], v[72:75], v[44:47]
	v_mfma_f32_16x16x32_bf16 v[48:51], v[170:173], v[72:75], v[48:51]
	v_add_u32_e32 v170, s1, v242
	s_add_i32 s1, s0, 1
	s_cmp_lg_u32 s0, 4
	v_mfma_f32_16x16x32_bf16 v[44:47], v[158:161], v[76:79], v[44:47]
	v_mfma_f32_16x16x32_bf16 v[48:51], v[162:165], v[76:79], v[48:51]
	v_mfma_f32_16x16x32_bf16 v[44:47], v[150:153], v[80:83], v[44:47]
	v_lshl_add_u64 v[150:151], v[148:149], 0, s[66:67]
	global_load_lds_dwordx4 v[150:151], off
	v_mfma_f32_16x16x32_bf16 v[48:51], v[154:157], v[80:83], v[48:51]
	ds_read_b128 v[150:153], v236 offset:50176
	ds_read_b128 v[154:157], v236 offset:49152
	ds_read_b128 v[158:161], v170
	ds_read_b128 v[162:165], v170 offset:1024
	ds_read_b128 v[166:169], v170 offset:2048
	ds_read_b128 v[170:173], v170 offset:3072
	ds_read_b128 v[174:177], v178 offset:8192
	ds_read_b128 v[178:181], v178 offset:9216
	s_waitcnt lgkmcnt(0)
	v_mfma_f32_16x16x32_bf16 v[144:147], v[174:177], v[158:161], v[144:147]
	v_mfma_f32_16x16x32_bf16 v[116:119], v[154:157], v[158:161], v[116:119]
	v_mfma_f32_16x16x32_bf16 v[104:107], v[178:181], v[158:161], v[104:107]
	v_mfma_f32_16x16x32_bf16 v[84:87], v[150:153], v[158:161], v[84:87]
	v_mfma_f32_16x16x32_bf16 v[88:91], v[174:177], v[162:165], v[88:91]
	v_mfma_f32_16x16x32_bf16 v[92:95], v[154:157], v[162:165], v[92:95]
	v_mfma_f32_16x16x32_bf16 v[96:99], v[178:181], v[162:165], v[96:99]
	v_mfma_f32_16x16x32_bf16 v[158:161], v[150:153], v[162:165], v[100:103]
	v_mfma_f32_16x16x32_bf16 v[108:111], v[174:177], v[166:169], v[108:111]
	v_mfma_f32_16x16x32_bf16 v[162:165], v[154:157], v[166:169], v[112:115]
	v_mfma_f32_16x16x32_bf16 v[182:185], v[178:181], v[166:169], v[120:123]
	v_mfma_f32_16x16x32_bf16 v[166:169], v[150:153], v[166:169], v[124:127]
	v_mfma_f32_16x16x32_bf16 v[174:177], v[174:177], v[170:173], v[128:131]
	v_mfma_f32_16x16x32_bf16 v[154:157], v[154:157], v[170:173], v[132:135]
	v_mfma_f32_16x16x32_bf16 v[178:181], v[178:181], v[170:173], v[136:139]
	v_mfma_f32_16x16x32_bf16 v[150:153], v[150:153], v[170:173], v[140:143]
	v_add_u32_e32 v170, s33, v234
	v_add_u32_e32 v171, s33, v231
	v_add_u32_e32 v172, s33, v227
	v_add_u32_e32 v173, s33, v229
	ds_read_b64_tr_b16 v[140:141], v170
	ds_read_b64_tr_b16 v[142:143], v171
	ds_read_b64_tr_b16 v[136:137], v172
	ds_read_b64_tr_b16 v[138:139], v173
	ds_read_b64_tr_b16 v[132:133], v170 offset:2048
	ds_read_b64_tr_b16 v[134:135], v171 offset:2048
	ds_read_b64_tr_b16 v[128:129], v172 offset:2048
	ds_read_b64_tr_b16 v[130:131], v173 offset:2048
	ds_read_b64_tr_b16 v[124:125], v170 offset:4096
	ds_read_b64_tr_b16 v[126:127], v171 offset:4096
	ds_read_b64_tr_b16 v[120:121], v172 offset:4096
	ds_read_b64_tr_b16 v[122:123], v173 offset:4096
	ds_read_b64_tr_b16 v[112:113], v170 offset:6144
	ds_read_b64_tr_b16 v[114:115], v171 offset:6144
	ds_read_b64_tr_b16 v[100:101], v172 offset:6144
	ds_read_b64_tr_b16 v[102:103], v173 offset:6144
	s_waitcnt lgkmcnt(0)
	s_cselect_b32 s33, s1, 0
	v_mfma_f32_16x16x32_bf16 v[56:59], v[136:139], v[68:71], v[56:59]
	s_lshl_b32 s0, s33, 14
	s_add_i32 s1, s0, 0xffffc000
	s_cmp_lg_u32 s33, 0
	v_mfma_f32_16x16x32_bf16 v[52:55], v[140:143], v[68:71], v[52:55]
	s_cselect_b32 s1, s1, 0x10000
	s_add_i32 s1, s1, 0
	s_waitcnt vmcnt(3)
	v_mfma_f32_16x16x32_bf16 v[56:59], v[128:131], v[72:75], v[56:59]
	s_add_i32 s1, s1, s44
	s_barrier
	v_mfma_f32_16x16x32_bf16 v[52:55], v[132:135], v[72:75], v[52:55]
	s_add_i32 m0, s1, 0x10000
	s_add_i32 s0, s86, s0
	v_mfma_f32_16x16x32_bf16 v[56:59], v[120:123], v[76:79], v[56:59]
	v_add_u32_e32 v120, s0, v242
	s_add_i32 s1, s0, 0x2000
	s_add_i32 s38, s33, 1
	v_mfma_f32_16x16x32_bf16 v[52:55], v[124:127], v[76:79], v[52:55]
	s_cmp_lg_u32 s33, 4
	v_mfma_f32_16x16x32_bf16 v[56:59], v[100:103], v[80:83], v[56:59]
	v_lshl_add_u64 v[100:101], v[148:149], 0, s[16:17]
	global_load_lds_dwordx4 v[100:101], off
	v_mfma_f32_16x16x32_bf16 v[52:55], v[112:115], v[80:83], v[52:55]
	ds_read_b128 v[170:173], v236 offset:58368
	ds_read_b128 v[186:189], v236 offset:57344
	ds_read_b128 v[100:103], v120
	ds_read_b128 v[112:115], v120 offset:1024
	ds_read_b128 v[190:193], v120 offset:2048
	ds_read_b128 v[194:197], v120 offset:3072
	v_add_u32_e32 v120, s0, v243
	ds_read_b128 v[202:205], v120 offset:8192
	ds_read_b128 v[208:211], v120 offset:9216
	s_waitcnt lgkmcnt(0)
	v_mfma_f32_16x16x32_bf16 v[140:143], v[202:205], v[100:103], v[144:147]
	v_mfma_f32_16x16x32_bf16 v[238:241], v[186:189], v[100:103], v[116:119]
	v_mfma_f32_16x16x32_bf16 v[132:135], v[208:211], v[100:103], v[104:107]
	v_mfma_f32_16x16x32_bf16 v[136:139], v[170:173], v[100:103], v[84:87]
	v_mfma_f32_16x16x32_bf16 v[104:107], v[202:205], v[112:115], v[88:91]
	v_mfma_f32_16x16x32_bf16 v[100:103], v[186:189], v[112:115], v[92:95]
	v_mfma_f32_16x16x32_bf16 v[124:127], v[208:211], v[112:115], v[96:99]
	v_mfma_f32_16x16x32_bf16 v[128:131], v[170:173], v[112:115], v[158:161]
	v_mfma_f32_16x16x32_bf16 v[120:123], v[186:189], v[190:193], v[162:165]
	v_mfma_f32_16x16x32_bf16 v[116:119], v[170:173], v[190:193], v[166:169]
	v_mfma_f32_16x16x32_bf16 v[92:95], v[202:205], v[194:197], v[174:177]
	v_mfma_f32_16x16x32_bf16 v[96:99], v[186:189], v[194:197], v[154:157]
	s_nop 1
	v_add_u32_e32 v176, s1, v234
	v_add_u32_e32 v177, s1, v231
	v_mov_b32_e32 v231, v3
	v_mfma_f32_16x16x32_bf16 v[84:87], v[208:211], v[194:197], v[178:181]
	v_mfma_f32_16x16x32_bf16 v[88:91], v[170:173], v[194:197], v[150:153]
	s_nop 1
	v_add_u32_e32 v178, s1, v227
	v_add_u32_e32 v179, s1, v229
	ds_read_b64_tr_b16 v[172:173], v176
	ds_read_b64_tr_b16 v[174:175], v177
	ds_read_b64_tr_b16 v[168:169], v178
	ds_read_b64_tr_b16 v[170:171], v179
	ds_read_b64_tr_b16 v[164:165], v176 offset:2048
	ds_read_b64_tr_b16 v[166:167], v177 offset:2048
	ds_read_b64_tr_b16 v[160:161], v178 offset:2048
	ds_read_b64_tr_b16 v[162:163], v179 offset:2048
	ds_read_b64_tr_b16 v[156:157], v176 offset:4096
	ds_read_b64_tr_b16 v[158:159], v177 offset:4096
	ds_read_b64_tr_b16 v[152:153], v178 offset:4096
	ds_read_b64_tr_b16 v[154:155], v179 offset:4096
	ds_read_b64_tr_b16 v[148:149], v176 offset:6144
	ds_read_b64_tr_b16 v[150:151], v177 offset:6144
	ds_read_b64_tr_b16 v[144:145], v178 offset:6144
	ds_read_b64_tr_b16 v[146:147], v179 offset:6144
	s_waitcnt lgkmcnt(0)
; #define LAS __attribute__((address_space(3)))
; template <int VAR  >
; __device__ __forceinline__ void ret_core_mfma(const bf16* P, const bf16* VT, const float* decay_logit  , bf16* YF, bf16* YB, float* PT, LAS unsigned char* lds, const int tid, const int bid, const int G) {
;     ...
; #pragma unroll
;             for (int m = 0; m < 4; ++m)
; #pragma unroll
;                 for (int n = 0; n < 2; ++n) { const int i = 64 * wr + 16 * m + frc;
;                     const float qdf = *(const LAS float*)(lds + RC_TB + 1536 + i * 4), rwf = *(const LAS float*)(lds + RC_TB + 512 + i * 4);
;                     const f32x4 clf = *(const LAS f32x4*)(lds + RC_TB + 1024 + (32 * wc + 16 * n + 4 * fqc) * 4);
;                     accY[m][n] = accY[m][n] * qdf;
; #pragma unroll
;                     for (int ii = 0; ii < 4; ++ii) { const int j = 32 * wc + 16 * n + 4 * fqc + ii; const int dd = dir ? j - i : i - j;
;                         accA[m][n][ii] = dd >= 0 ? accA[m][n][ii] * (rwf * clf[ii]) : 0.f; } }
	v_mfma_f32_16x16x32_bf16 v[112:115], v[202:205], v[190:193], v[108:111]
	v_ashrrev_i32_e32 v229, 31, v228
	v_ashrrev_i32_e32 v227, 31, v226
	v_mfma_f32_16x16x32_bf16 v[60:63], v[172:175], v[68:71], v[60:63]
	v_mfma_f32_16x16x32_bf16 v[64:67], v[168:171], v[68:71], v[64:67]
	v_mfma_f32_16x16x32_bf16 v[60:63], v[164:167], v[72:75], v[60:63]
	v_mfma_f32_16x16x32_bf16 v[64:67], v[160:163], v[72:75], v[64:67]
	v_mfma_f32_16x16x32_bf16 v[60:63], v[156:159], v[76:79], v[60:63]
	v_mfma_f32_16x16x32_bf16 v[64:67], v[152:155], v[76:79], v[64:67]
	v_mfma_f32_16x16x32_bf16 v[60:63], v[148:151], v[80:83], v[60:63]
	v_or_b32_e32 v149, s77, v2
	v_lshlrev_b32_e32 v68, 2, v149
	v_add_u32_e32 v69, s35, v68
	v_mfma_f32_16x16x32_bf16 v[64:67], v[144:147], v[80:83], v[64:67]
	v_lshl_add_u32 v144, v215, 2, s82
	ds_read_b32 v72, v69
	v_add_u32_e32 v68, s64, v68
	ds_read_b32 v150, v68
	v_lshl_add_u32 v68, v144, 2, s65
	ds_read_b128 v[76:79], v68
	s_waitcnt lgkmcnt(0)
	v_pk_mul_f32 v[70:71], v[240:241], v[72:73] op_sel_hi:[1,0]
	v_pk_mul_f32 v[68:69], v[238:239], v[72:73] op_sel_hi:[1,0]
	v_sub_u32_e32 v73, v144, v149
	v_sub_u32_e32 v74, v149, v144
	v_cndmask_b32_e64 v73, v73, v74, s[4:5]
	v_cmp_lt_i32_e32 vcc, -1, v73
	v_mul_f32_e32 v73, v150, v76
	v_mul_f32_e32 v73, v140, v73
	v_or_b32_e32 v145, 1, v144
	v_cndmask_b32_e32 v140, 0, v73, vcc
	v_sub_u32_e32 v73, v145, v149
	v_sub_u32_e32 v74, v149, v145
	v_cndmask_b32_e64 v73, v73, v74, s[4:5]
	v_cmp_lt_i32_e64 s[0:1], -1, v73
	v_mul_f32_e32 v73, v150, v77
	v_mul_f32_e32 v73, v141, v73
	v_or_b32_e32 v146, 2, v144
	v_cndmask_b32_e64 v141, 0, v73, s[0:1]
	v_sub_u32_e32 v73, v146, v149
	v_sub_u32_e32 v74, v149, v146
	v_cndmask_b32_e64 v73, v73, v74, s[4:5]
	v_cmp_lt_i32_e64 s[0:1], -1, v73
	v_mul_f32_e32 v73, v150, v78
	v_mul_f32_e32 v73, v142, v73
	v_or_b32_e32 v147, 3, v144
	v_cndmask_b32_e64 v142, 0, v73, s[0:1]
	v_sub_u32_e32 v73, v147, v149
	v_sub_u32_e32 v74, v149, v147
	v_cndmask_b32_e64 v73, v73, v74, s[4:5]
	v_cmp_lt_i32_e64 s[0:1], -1, v73
	v_mul_f32_e32 v73, v150, v79
	v_mul_f32_e32 v73, v143, v73
	v_add_u32_e32 v148, 16, v144
	v_cndmask_b32_e64 v143, 0, v73, s[0:1]
	v_lshl_add_u32 v73, v148, 2, s65
	ds_read_b128 v[80:83], v73
	v_pk_mul_f32 v[74:75], v[138:139], v[72:73] op_sel_hi:[1,0]
	v_pk_mul_f32 v[72:73], v[136:137], v[72:73] op_sel_hi:[1,0]
	v_sub_u32_e32 v136, v148, v149
	v_sub_u32_e32 v137, v149, v148
	v_cndmask_b32_e64 v136, v136, v137, s[4:5]
	v_cmp_lt_i32_e64 s[0:1], -1, v136
	s_waitcnt lgkmcnt(0)
	v_mul_f32_e32 v136, v150, v80
	v_add_u32_e32 v138, 17, v144
	v_mul_f32_e32 v132, v132, v136
	v_sub_u32_e32 v136, v138, v149
	v_sub_u32_e32 v137, v149, v138
	v_cndmask_b32_e64 v136, v136, v137, s[4:5]
	v_cndmask_b32_e64 v132, 0, v132, s[0:1]
	v_cmp_lt_i32_e64 s[0:1], -1, v136
	v_mul_f32_e32 v136, v150, v81
	v_add_u32_e32 v137, 18, v144
	v_mul_f32_e32 v133, v133, v136
	v_sub_u32_e32 v136, v137, v149
	v_sub_u32_e32 v139, v149, v137
	v_cndmask_b32_e64 v136, v136, v139, s[4:5]
	v_cndmask_b32_e64 v133, 0, v133, s[0:1]
	v_cmp_lt_i32_e64 s[0:1], -1, v136
	v_mul_f32_e32 v136, v150, v82
	v_mul_f32_e32 v134, v134, v136
	v_add_u32_e32 v136, 19, v144
	v_sub_u32_e32 v139, v136, v149
	v_sub_u32_e32 v151, v149, v136
	v_cndmask_b32_e64 v139, v139, v151, s[4:5]
	v_cndmask_b32_e64 v134, 0, v134, s[0:1]
	v_cmp_lt_i32_e64 s[0:1], -1, v139
	v_mul_f32_e32 v139, v150, v83
	v_or_b32_e32 v153, 16, v149
	v_mul_f32_e32 v135, v135, v139
	v_lshlrev_b32_e32 v139, 2, v153
	v_add_u32_e32 v150, s35, v139
	v_add_u32_e32 v139, s64, v139
	ds_read_b32 v154, v150
	ds_read_b32 v155, v139
	v_sub_u32_e32 v139, v144, v153
	v_sub_u32_e32 v150, v153, v144
	v_cndmask_b32_e64 v139, v139, v150, s[4:5]
	v_cndmask_b32_e64 v135, 0, v135, s[0:1]
	v_cmp_lt_i32_e64 s[0:1], -1, v139
	s_waitcnt lgkmcnt(0)
	v_mul_f32_e32 v139, v76, v155
	v_mul_f32_e32 v104, v104, v139
	v_cndmask_b32_e64 v139, 0, v104, s[0:1]
	v_sub_u32_e32 v104, v145, v153
	v_sub_u32_e32 v150, v153, v145
	v_cndmask_b32_e64 v104, v104, v150, s[4:5]
	v_cmp_lt_i32_e64 s[0:1], -1, v104
	v_mul_f32_e32 v104, v77, v155
	v_mul_f32_e32 v104, v105, v104
	v_cndmask_b32_e64 v150, 0, v104, s[0:1]
	v_sub_u32_e32 v104, v146, v153
	v_sub_u32_e32 v105, v153, v146
	v_cndmask_b32_e64 v104, v104, v105, s[4:5]
	v_cmp_lt_i32_e64 s[0:1], -1, v104
	v_mul_f32_e32 v104, v78, v155
	v_mul_f32_e32 v104, v106, v104
	v_cndmask_b32_e64 v151, 0, v104, s[0:1]
	v_sub_u32_e32 v104, v147, v153
	v_sub_u32_e32 v105, v153, v147
	v_cndmask_b32_e64 v104, v104, v105, s[4:5]
	v_cmp_lt_i32_e64 s[0:1], -1, v104
	v_mul_f32_e32 v104, v79, v155
	v_mul_f32_e32 v104, v107, v104
	v_cndmask_b32_e64 v152, 0, v104, s[0:1]
	v_pk_mul_f32 v[104:105], v[128:129], v[154:155] op_sel_hi:[1,0]
	v_mul_f32_e32 v128, v80, v155
	v_mul_f32_e32 v124, v124, v128
	v_cndmask_b32_e32 v128, 0, v124, vcc
	v_sub_u32_e32 v124, v138, v153
	v_sub_u32_e32 v129, v153, v138
	v_cndmask_b32_e64 v124, v124, v129, s[4:5]
	v_cmp_lt_i32_e32 vcc, -1, v124
	v_mul_f32_e32 v124, v81, v155
	v_mul_f32_e32 v124, v125, v124
	v_cndmask_b32_e32 v125, 0, v124, vcc
	v_sub_u32_e32 v124, v137, v153
	v_sub_u32_e32 v129, v153, v137
	v_cndmask_b32_e64 v124, v124, v129, s[4:5]
	v_cmp_lt_i32_e32 vcc, -1, v124
	v_mul_f32_e32 v124, v82, v155
	v_mul_f32_e32 v124, v126, v124
	v_cndmask_b32_e32 v126, 0, v124, vcc
	v_sub_u32_e32 v124, v136, v153
	v_sub_u32_e32 v129, v153, v136
	v_cndmask_b32_e64 v124, v124, v129, s[4:5]
	v_pk_mul_f32 v[102:103], v[102:103], v[154:155] op_sel_hi:[1,0]
	v_pk_mul_f32 v[100:101], v[100:101], v[154:155] op_sel_hi:[1,0]
	v_pk_mul_f32 v[106:107], v[130:131], v[154:155] op_sel_hi:[1,0]
	v_cmp_lt_i32_e32 vcc, -1, v124
	v_mul_f32_e32 v124, v83, v155
	v_or_b32_e32 v154, 32, v149
	v_mul_f32_e32 v124, v127, v124
	v_lshlrev_b32_e32 v129, 2, v154
	v_cndmask_b32_e32 v127, 0, v124, vcc
	v_add_u32_e32 v124, s35, v129
	v_add_u32_e32 v129, s64, v129
	ds_read_b32 v124, v124
	ds_read_b32 v155, v129
	v_sub_u32_e32 v129, v144, v154
	v_sub_u32_e32 v130, v154, v144
	v_cndmask_b32_e64 v129, v129, v130, s[4:5]
	v_cmp_lt_i32_e32 vcc, -1, v129
	s_waitcnt lgkmcnt(0)
; #define LAS __attribute__((address_space(3)))
; __device__ __forceinline__ unsigned cvtpk(float lo, float hi) { f32x2_t v = {lo, hi}; bf16x2_t b = __builtin_convertvector(v, bf16x2_t); return __builtin_bit_cast(unsigned, b); }
; #define RC_WAITV(n) asm volatile("s_waitcnt vmcnt(" #n ")" ::: "memory")
; #define RC_WAITL() asm volatile("s_waitcnt lgkmcnt(0)" ::: "memory")
; #define RC_BAR() do { asm volatile("" ::: "memory"); __builtin_amdgcn_s_barrier(); asm volatile("" ::: "memory"); } while (0)
; template <int VAR  >
; __device__ __forceinline__ void ret_core_mfma(const bf16* P, const bf16* VT, const float* decay_logit  , bf16* YF, bf16* YB, float* PT, LAS unsigned char* lds, const int tid, const int bid, const int G) {
;     ...
; #pragma unroll
;             for (int m = 0; m < 4; ++m)
; #pragma unroll
;                 for (int n = 0; n < 2; ++n) { const int i = 64 * wr + 16 * m + frc;
;                     const float qdf = *(const LAS float*)(lds + RC_TB + 1536 + i * 4), rwf = *(const LAS float*)(lds + RC_TB + 512 + i * 4);
;                     const f32x4 clf = *(const LAS f32x4*)(lds + RC_TB + 1024 + (32 * wc + 16 * n + 4 * fqc) * 4);
;                     accY[m][n] = accY[m][n] * qdf;
; #pragma unroll
;                     for (int ii = 0; ii < 4; ++ii) { const int j = 32 * wc + 16 * n + 4 * fqc + ii; const int dd = dir ? j - i : i - j;
;                         accA[m][n][ii] = dd >= 0 ? accA[m][n][ii] * (rwf * clf[ii]) : 0.f; } }
;             RC_BAR();
; #pragma unroll
;             for (int m = 0; m < 4; ++m)
; #pragma unroll
;                 for (int n = 0; n < 2; ++n) { v2u pw; pw.x = cvtpk(accA[m][n][0], accA[m][n][1]); pw.y = cvtpk(accA[m][n][2], accA[m][n][3]);
;                     *(LAS v2u*)(lds + RC_ST + wc * 8192 + (4 * wr + m) * 1024 + sl_swz(frc * 64 + (16 * n + 4 * fqc) * 2)) = pw; }
; #pragma unroll
;             for (int js = 0; js < 4; ++js) vnx[js] = *(const v4u*)(vown + tokn + 32 * js + zo);
;             RC_WAITL();
; #pragma unroll
;             for (int js = 0; js < 4; ++js) {
;                 if (js == 0) RC_WAITV(7); else if (js == 1) RC_WAITV(8); else if (js == 2) RC_WAITV(9); else RC_WAITV(10);
;                 RC_BAR();
	v_mul_f32_e32 v129, v76, v155
	v_mul_f32_e32 v112, v112, v129
	v_cndmask_b32_e32 v129, 0, v112, vcc
	v_sub_u32_e32 v112, v145, v154
	v_sub_u32_e32 v130, v154, v145
	v_cndmask_b32_e64 v112, v112, v130, s[4:5]
	v_cmp_lt_i32_e32 vcc, -1, v112
	v_mul_f32_e32 v112, v77, v155
	v_mul_f32_e32 v112, v113, v112
	v_cndmask_b32_e32 v130, 0, v112, vcc
	v_sub_u32_e32 v112, v146, v154
	v_sub_u32_e32 v113, v154, v146
	v_cndmask_b32_e64 v112, v112, v113, s[4:5]
	v_cmp_lt_i32_e32 vcc, -1, v112
	v_mul_f32_e32 v112, v78, v155
	v_mul_f32_e32 v112, v114, v112
	v_cndmask_b32_e32 v131, 0, v112, vcc
	v_sub_u32_e32 v112, v147, v154
	v_sub_u32_e32 v113, v154, v147
	v_cndmask_b32_e64 v112, v112, v113, s[4:5]
	v_cmp_lt_i32_e32 vcc, -1, v112
	v_mul_f32_e32 v112, v79, v155
	v_mfma_f32_16x16x32_bf16 v[108:111], v[208:211], v[190:193], v[182:185]
	v_mul_f32_e32 v112, v115, v112
	v_cndmask_b32_e32 v153, 0, v112, vcc
	v_pk_mul_f32 v[112:113], v[116:117], v[124:125] op_sel_hi:[1,0]
	v_sub_u32_e32 v116, v148, v154
	v_sub_u32_e32 v117, v154, v148
	v_cndmask_b32_e64 v116, v116, v117, s[4:5]
	v_cmp_lt_i32_e32 vcc, -1, v116
	v_mul_f32_e32 v116, v80, v155
	v_mul_f32_e32 v108, v108, v116
	v_sub_u32_e32 v116, v138, v154
	v_sub_u32_e32 v117, v154, v138
	v_cndmask_b32_e64 v116, v116, v117, s[4:5]
	v_cndmask_b32_e32 v108, 0, v108, vcc
	v_cmp_lt_i32_e32 vcc, -1, v116
	v_mul_f32_e32 v116, v81, v155
	v_mul_f32_e32 v109, v109, v116
	v_sub_u32_e32 v116, v137, v154
	v_sub_u32_e32 v117, v154, v137
	v_cndmask_b32_e64 v116, v116, v117, s[4:5]
	v_cndmask_b32_e32 v109, 0, v109, vcc
	v_cmp_lt_i32_e32 vcc, -1, v116
	v_mul_f32_e32 v116, v82, v155
	v_mul_f32_e32 v110, v110, v116
	v_sub_u32_e32 v116, v136, v154
	v_sub_u32_e32 v117, v154, v136
	v_cndmask_b32_e64 v116, v116, v117, s[4:5]
	v_or_b32_e32 v117, 48, v149
	v_pk_mul_f32 v[114:115], v[118:119], v[124:125] op_sel_hi:[1,0]
	v_cndmask_b32_e32 v110, 0, v110, vcc
	v_cmp_lt_i32_e32 vcc, -1, v116
	v_mul_f32_e32 v116, v83, v155
	v_lshlrev_b32_e32 v118, 2, v117
	v_mul_f32_e32 v111, v111, v116
	v_add_u32_e32 v116, s35, v118
	v_add_u32_e32 v118, s64, v118
	ds_read_b32 v116, v116
	ds_read_b32 v118, v118
	v_pk_mul_f32 v[122:123], v[122:123], v[124:125] op_sel_hi:[1,0]
	v_pk_mul_f32 v[120:121], v[120:121], v[124:125] op_sel_hi:[1,0]
	v_sub_u32_e32 v119, v144, v117
	v_sub_u32_e32 v124, v117, v144
	v_cndmask_b32_e64 v119, v119, v124, s[4:5]
	s_waitcnt lgkmcnt(0)
	v_mul_f32_e32 v76, v76, v118
	v_cndmask_b32_e32 v111, 0, v111, vcc
	v_cmp_lt_i32_e32 vcc, -1, v119
	v_mul_f32_e32 v76, v92, v76
	v_sub_u32_e32 v92, v117, v145
	v_cndmask_b32_e32 v119, 0, v76, vcc
	v_sub_u32_e32 v76, v145, v117
	v_cndmask_b32_e64 v76, v76, v92, s[4:5]
	v_cmp_lt_i32_e32 vcc, -1, v76
	v_mul_f32_e32 v76, v77, v118
	v_mul_f32_e32 v76, v93, v76
	v_cndmask_b32_e32 v124, 0, v76, vcc
	v_sub_u32_e32 v76, v146, v117
	v_sub_u32_e32 v77, v117, v146
	v_cndmask_b32_e64 v76, v76, v77, s[4:5]
	v_cmp_lt_i32_e32 vcc, -1, v76
	v_mul_f32_e32 v76, v78, v118
	v_mul_f32_e32 v76, v94, v76
	v_cndmask_b32_e32 v78, 0, v76, vcc
	v_sub_u32_e32 v76, v147, v117
	v_sub_u32_e32 v77, v117, v147
	v_cndmask_b32_e64 v76, v76, v77, s[4:5]
	v_cmp_lt_i32_e32 vcc, -1, v76
	v_mul_f32_e32 v76, v79, v118
	v_mul_f32_e32 v76, v95, v76
	v_cndmask_b32_e32 v79, 0, v76, vcc
	v_sub_u32_e32 v76, v148, v117
	v_sub_u32_e32 v77, v117, v148
	v_cndmask_b32_e64 v76, v76, v77, s[4:5]
	v_cmp_lt_i32_e32 vcc, -1, v76
	v_mul_f32_e32 v76, v80, v118
	v_mul_f32_e32 v76, v84, v76
	v_cndmask_b32_e32 v80, 0, v76, vcc
	v_sub_u32_e32 v76, v138, v117
	v_sub_u32_e32 v77, v117, v138
	v_cndmask_b32_e64 v76, v76, v77, s[4:5]
	v_cmp_lt_i32_e32 vcc, -1, v76
	v_mul_f32_e32 v76, v81, v118
	v_mul_f32_e32 v76, v85, v76
	v_cndmask_b32_e32 v81, 0, v76, vcc
	v_sub_u32_e32 v76, v137, v117
	v_sub_u32_e32 v77, v117, v137
	v_cndmask_b32_e64 v76, v76, v77, s[4:5]
	v_cmp_lt_i32_e32 vcc, -1, v76
	v_mul_f32_e32 v76, v82, v118
	v_mul_f32_e32 v76, v86, v76
	v_lshl_add_u32 v84, v2, 6, v226
	v_cndmask_b32_e32 v82, 0, v76, vcc
	v_sub_u32_e32 v76, v136, v117
	v_sub_u32_e32 v77, v117, v136
	v_lshrrev_b32_e32 v85, 4, v84
	v_cndmask_b32_e64 v76, v76, v77, s[4:5]
	v_and_b32_e32 v85, 32, v85
	v_cmp_lt_i32_e32 vcc, -1, v76
	v_mul_f32_e32 v76, v83, v118
	v_xad_u32 v85, v85, v84, s83
	v_add_u32_e32 v84, 32, v84
	v_mul_f32_e32 v76, v87, v76
	v_lshrrev_b32_e32 v86, 4, v84
	v_cndmask_b32_e32 v83, 0, v76, vcc
	v_cvt_pk_bf16_f32 v76, v140, v141
	v_cvt_pk_bf16_f32 v77, v142, v143
	v_and_b32_e32 v86, 32, v86
	ds_write_b64 v85, v[76:77]
	v_cvt_pk_bf16_f32 v76, v132, v133
	v_cvt_pk_bf16_f32 v77, v134, v135
	v_xad_u32 v84, v86, v84, s83
	ds_write_b64 v84, v[76:77]
	v_cvt_pk_bf16_f32 v76, v139, v150
	v_cvt_pk_bf16_f32 v77, v151, v152
	ds_write_b64 v85, v[76:77] offset:1024
	v_cvt_pk_bf16_f32 v76, v128, v125
	v_cvt_pk_bf16_f32 v77, v126, v127
	ds_write_b64 v84, v[76:77] offset:1024
	v_cvt_pk_bf16_f32 v76, v129, v130
	v_cvt_pk_bf16_f32 v77, v131, v153
	ds_write_b64 v85, v[76:77] offset:2048
	v_cvt_pk_bf16_f32 v76, v108, v109
	v_cvt_pk_bf16_f32 v77, v110, v111
	s_cselect_b32 s0, s38, 0
	ds_write_b64 v84, v[76:77] offset:2048
	v_cvt_pk_bf16_f32 v76, v119, v124
	v_cvt_pk_bf16_f32 v77, v78, v79
	s_lshl_b32 s40, s7, 7
	ds_write_b64 v85, v[76:77] offset:3072
	v_cvt_pk_bf16_f32 v76, v80, v81
	v_cvt_pk_bf16_f32 v77, v82, v83
	s_ashr_i32 s41, s40, 31
	s_lshl_b32 s1, s0, 14
	ds_write_b64 v84, v[76:77] offset:3072
	v_lshl_add_u64 v[76:77], s[40:41], 1, v[222:223]
	s_lshl_b64 s[40:41], s[40:41], 12
	s_add_i32 s7, s1, 0xc000
	v_lshl_add_u64 v[80:81], v[228:229], 1, v[76:77]
	s_cmp_lg_u32 s0, 0
	v_pk_mul_f32 v[94:95], v[90:91], v[116:117] op_sel_hi:[1,0]
	v_pk_mul_f32 v[92:93], v[88:89], v[116:117] op_sel_hi:[1,0]
	global_load_dwordx4 v[88:91], v[80:81], off
	global_load_dwordx4 v[84:87], v[80:81], off offset:64
	global_load_dwordx4 v[76:79], v[80:81], off offset:128
	s_nop 0
	global_load_dwordx4 v[80:83], v[80:81], off offset:192
	s_waitcnt lgkmcnt(0)
	s_cselect_b32 s7, s7, 0x20000
	s_waitcnt vmcnt(7)
	s_add_i32 s7, s45, s7
	s_barrier
; #define LAS __attribute__((address_space(3)))
; #define RC_WAITV(n) asm volatile("s_waitcnt vmcnt(" #n ")" ::: "memory")
; #define RC_WAITL() asm volatile("s_waitcnt lgkmcnt(0)" ::: "memory")
; #define RC_BAR() do { asm volatile("" ::: "memory"); __builtin_amdgcn_s_barrier(); asm volatile("" ::: "memory"); } while (0)
; #define RC_MFMA(b, a, c) __builtin_amdgcn_mfma_f32_16x16x32_bf16((b), (a), (c), 0, 0, 0)
; #define RC_ISSUE(st, tk, sl) do { if ((st) < 8) { const size_t to_ = (size_t)(tk) * RQK + 32 * (st); RC_DMA(qsrc + to_, RC_RG + (sl) * 16384 + w * 1024); RC_DMA(ksrc + to_, RC_RG + (sl) * 16384 + 8192 + w * 1024); } \
;                                   else RC_DMA(vsrc + (tk) + 32 * ((st) - 8), RC_RG + (sl) * 16384 + w * 1024); } while (0)
; template <int VAR  >
; __device__ __forceinline__ void ret_core_mfma(const bf16* P, const bf16* VT, const float* decay_logit  , bf16* YF, bf16* YB, float* PT, LAS unsigned char* lds, const int tid, const int bid, const int G) {
;     ...
;             for (int js = 0; js < 4; ++js) {
;                 if (js == 0) RC_WAITV(7); else if (js == 1) RC_WAITV(8); else if (js == 2) RC_WAITV(9); else RC_WAITV(10);
;                 RC_BAR();
;                 { const int s4 = RC_PREV(slot); RC_ISSUE(js, tokn, s4); }
;                 bf16x8v At[4], Bv[2];
;                 const LAS unsigned char* sv = lds + RC_RG + slot * 16384;
; #pragma unroll
;                 for (int m = 0; m < 4; ++m) At[m] = *(const LAS bf16x8v*)(lds + RC_ST + js * 8192 + aoff + m * 1024);
; #pragma unroll
;                 for (int n = 0; n < 2; ++n) Bv[n] = *(const LAS bf16x8v*)(sv + boff + n * 1024);
;                 RC_WAITL();
; #pragma unroll
;                 for (int m = 0; m < 4; ++m)
; #pragma unroll
;                     for (int n = 0; n < 2; ++n) accY[m][n] = RC_MFMA(Bv[n], At[m], accY[m][n]);
;                 slot = RC_NEXT(slot);
	v_add_u32_e32 v144, 0, v242
	v_add_u32_e32 v110, s1, v251
	s_add_i32 s1, s0, 1
	s_cmp_lg_u32 s0, 4
	s_cselect_b32 s0, s1, 0
	v_pk_mul_f32 v[98:99], v[98:99], v[116:117] op_sel_hi:[1,0]
	v_pk_mul_f32 v[96:97], v[96:97], v[116:117] op_sel_hi:[1,0]
	ds_read_b128 v[116:119], v144
	ds_read_b128 v[124:127], v144 offset:1024
	ds_read_b128 v[128:131], v144 offset:2048
	ds_read_b128 v[132:135], v144 offset:3072
	ds_read_b128 v[136:139], v110
	ds_read_b128 v[140:143], v110 offset:1024
	v_lshl_add_u64 v[108:109], v[218:219], 0, s[40:41]
	s_mov_b32 m0, s7
	v_lshl_add_u64 v[110:111], v[108:109], 0, s[62:63]
	global_load_lds_dwordx4 v[108:109], off
	s_add_i32 m0, s7, 0x2000
	s_nop 0
	global_load_lds_dwordx4 v[110:111], off
	s_lshl_b32 s1, s0, 14
	s_add_i32 s7, s1, 0xc000
	s_cmp_lg_u32 s0, 0
	s_waitcnt lgkmcnt(0)
	s_cselect_b32 s7, s7, 0x20000
	s_waitcnt vmcnt(8)
	s_add_i32 s7, s45, s7
	s_waitcnt lgkmcnt(0)
	v_mfma_f32_16x16x32_bf16 v[110:113], v[140:143], v[128:131], v[112:115]
	s_barrier
	s_mov_b32 m0, s7
	v_mfma_f32_16x16x32_bf16 v[68:71], v[136:139], v[116:119], v[68:71]
	v_lshl_add_u64 v[114:115], v[108:109], 0, 64
	global_load_lds_dwordx4 v[114:115], off
	v_lshl_add_u64 v[114:115], v[108:109], 0, s[72:73]
	s_add_i32 m0, s7, 0x2000
	v_mfma_f32_16x16x32_bf16 v[72:75], v[140:143], v[116:119], v[72:75]
	global_load_lds_dwordx4 v[114:115], off
	v_add_u32_e32 v114, s1, v251
	s_add_i32 s1, s0, 1
	s_cmp_lg_u32 s0, 4
	s_cselect_b32 s0, s1, 0
	s_lshl_b32 s1, s0, 14
	v_mfma_f32_16x16x32_bf16 v[100:103], v[136:139], v[124:127], v[100:103]
	s_add_i32 s7, s1, 0xc000
	s_cmp_lg_u32 s0, 0
	s_cselect_b32 s7, s7, 0x20000
	v_mfma_f32_16x16x32_bf16 v[104:107], v[140:143], v[124:127], v[104:107]
	s_add_i32 s7, s45, s7
	s_mov_b32 m0, s7
	v_mfma_f32_16x16x32_bf16 v[116:119], v[136:139], v[128:131], v[120:123]
	v_mfma_f32_16x16x32_bf16 v[96:99], v[136:139], v[132:135], v[96:99]
	v_mfma_f32_16x16x32_bf16 v[92:95], v[140:143], v[132:135], v[92:95]
	s_nop 0
	ds_read_b128 v[120:123], v144 offset:8192
	ds_read_b128 v[124:127], v144 offset:9216
	ds_read_b128 v[128:131], v144 offset:10240
	ds_read_b128 v[132:135], v144 offset:11264
	ds_read_b128 v[136:139], v114
	ds_read_b128 v[140:143], v114 offset:1024
	s_waitcnt lgkmcnt(0)
	s_waitcnt vmcnt(9)
	s_waitcnt lgkmcnt(0)
	v_mfma_f32_16x16x32_bf16 v[114:117], v[136:139], v[128:131], v[116:119]
	s_barrier
	v_mfma_f32_16x16x32_bf16 v[68:71], v[136:139], v[120:123], v[68:71]
	s_nop 0
	v_lshl_add_u64 v[118:119], v[108:109], 0, s[66:67]
	global_load_lds_dwordx4 v[118:119], off
	v_mfma_f32_16x16x32_bf16 v[100:103], v[136:139], v[124:127], v[100:103]
	s_add_i32 m0, s7, 0x2000
	v_lshl_add_u64 v[118:119], v[108:109], 0, s[84:85]
	global_load_lds_dwordx4 v[118:119], off
	v_mfma_f32_16x16x32_bf16 v[96:99], v[136:139], v[132:135], v[96:99]
	v_add_u32_e32 v138, s1, v251
	s_add_i32 s1, s0, 1
	s_cmp_lg_u32 s0, 4
	s_cselect_b32 s7, s1, 0
	v_mfma_f32_16x16x32_bf16 v[72:75], v[140:143], v[120:123], v[72:75]
	s_lshl_b32 s0, s7, 14
	s_add_i32 s1, s0, 0xc000
	s_cmp_lg_u32 s7, 0
	v_mfma_f32_16x16x32_bf16 v[104:107], v[140:143], v[124:127], v[104:107]
	s_cselect_b32 s1, s1, 0x20000
	s_add_i32 s1, s45, s1
	s_mov_b32 m0, s1
	v_mfma_f32_16x16x32_bf16 v[110:113], v[140:143], v[128:131], v[110:113]
	v_mfma_f32_16x16x32_bf16 v[92:95], v[140:143], v[132:135], v[92:95]
	ds_read_b128 v[118:121], v144 offset:16384
	ds_read_b128 v[122:125], v144 offset:17408
	ds_read_b128 v[126:129], v144 offset:18432
	ds_read_b128 v[130:133], v144 offset:19456
	ds_read_b128 v[134:137], v138
	ds_read_b128 v[138:141], v138 offset:1024
	s_waitcnt lgkmcnt(0)
	s_waitcnt vmcnt(10)
	s_waitcnt lgkmcnt(0)
	v_mfma_f32_16x16x32_bf16 v[114:117], v[134:137], v[126:129], v[114:117]
	s_barrier
; #define LAS __attribute__((address_space(3)))
; template <int O> __device__ __forceinline__ float swz_xor(float v) { return __builtin_bit_cast(float, __builtin_amdgcn_ds_swizzle(__builtin_bit_cast(int, v), (O << 10) | 0x1f)); }
; template <int VAR  >
; __device__ __forceinline__ void ret_core_mfma(const bf16* P, const bf16* VT, const float* decay_logit  , bf16* YF, bf16* YB, float* PT, LAS unsigned char* lds, const int tid, const int bid, const int G) {
;     ...
;             for (int js = 0; js < 4; ++js) {
;                 if (js == 0) RC_WAITV(7); else if (js == 1) RC_WAITV(8); else if (js == 2) RC_WAITV(9); else RC_WAITV(10);
;                 RC_BAR();
;                 { const int s4 = RC_PREV(slot); RC_ISSUE(js, tokn, s4); }
;                 bf16x8v At[4], Bv[2];
;                 const LAS unsigned char* sv = lds + RC_RG + slot * 16384;
; #pragma unroll
;                 for (int m = 0; m < 4; ++m) At[m] = *(const LAS bf16x8v*)(lds + RC_ST + js * 8192 + aoff + m * 1024);
; #pragma unroll
;                 for (int n = 0; n < 2; ++n) Bv[n] = *(const LAS bf16x8v*)(sv + boff + n * 1024);
;                 RC_WAITL();
; #pragma unroll
;                 for (int m = 0; m < 4; ++m)
; #pragma unroll
;                     for (int n = 0; n < 2; ++n) accY[m][n] = RC_MFMA(Bv[n], At[m], accY[m][n]);
;                 slot = RC_NEXT(slot);
;             }
; #pragma unroll
;             for (int m = 0; m < 4; ++m) { v4u pw; pw.x = cvtpk(accY[m][0][0], accY[m][0][1]); pw.y = cvtpk(accY[m][0][2], accY[m][0][3]); pw.z = cvtpk(accY[m][1][0], accY[m][1][1]); pw.w = cvtpk(accY[m][1][2], accY[m][1][3]);
;                 *(v4u*)(Y + (rowbase + tok0 + 64 * wr + 16 * m + frc + zo) * DV + h * DVR + es * 128 + 32 * wc + 8 * fqc) = pw; }
; #pragma unroll
;             for (int m = 0; m < 4; ++m) { float sv = 0.f, sq = 0.f;
; #pragma unroll
;                 for (int n = 0; n < 2; ++n)
; #pragma unroll
;                     for (int ii = 0; ii < 4; ++ii) { const float yv = accY[m][n][ii]; sv += yv; sq += yv * yv; }
;                 sv += swz_xor<16>(sv); sq += swz_xor<16>(sq); sv += get_xor32(sv, lc); sq += get_xor32(sq, lc);
;                 float* sp = PT + (((size_t)((h * 2 + dir) * 16 + es * 4 + wc)) * M + (rowbase + tok0 + 64 * wr + 16 * m + frc + zo)) * 2;
;                 if (fqc == 0) *(f32x2_t*)sp = (f32x2_t){sv, sq}; }
	v_mfma_f32_16x16x32_bf16 v[110:113], v[138:141], v[126:129], v[110:113]
	v_mfma_f32_16x16x32_bf16 v[126:129], v[138:141], v[130:133], v[92:95]
	s_nop 2
	v_lshl_add_u64 v[92:93], v[108:109], 0, s[16:17]
	global_load_lds_dwordx4 v[92:93], off
	v_lshl_add_u64 v[92:93], v[108:109], 0, s[18:19]
	s_add_i32 m0, s1, 0x2000
	v_mfma_f32_16x16x32_bf16 v[68:71], v[134:137], v[118:121], v[68:71]
	global_load_lds_dwordx4 v[92:93], off
	v_mfma_f32_16x16x32_bf16 v[72:75], v[138:141], v[118:121], v[72:75]
	v_mfma_f32_16x16x32_bf16 v[118:121], v[138:141], v[122:125], v[104:107]
	s_nop 2
	v_add_u32_e32 v104, s0, v251
	v_mfma_f32_16x16x32_bf16 v[100:103], v[134:137], v[122:125], v[100:103]
	s_add_u32 s0, s60, s53
	s_addc_u32 s1, s93, 0
	v_lshl_add_u64 v[108:109], s[0:1], 0, v[228:229]
	v_mfma_f32_16x16x32_bf16 v[122:125], v[134:137], v[130:133], v[96:99]
	ds_read_b128 v[92:95], v144 offset:24576
	s_nop 1
	ds_read_b128 v[96:99], v144 offset:25600
	ds_read_b128 v[130:133], v144 offset:26624
	ds_read_b128 v[134:137], v144 offset:27648
	ds_read_b128 v[138:141], v104
	ds_read_b128 v[142:145], v104 offset:1024
	s_waitcnt lgkmcnt(0)
	s_waitcnt lgkmcnt(0)
	v_mfma_f32_16x16x32_bf16 v[146:149], v[138:141], v[92:95], v[68:71]
	s_mov_b32 s0, 0x30000
	v_mfma_f32_16x16x32_bf16 v[150:153], v[142:145], v[92:95], v[72:75]
	v_mfma_f32_16x16x32_bf16 v[104:107], v[138:141], v[96:99], v[100:103]
	v_mfma_f32_16x16x32_bf16 v[100:103], v[142:145], v[96:99], v[118:121]
	v_mfma_f32_16x16x32_bf16 v[92:95], v[142:145], v[130:133], v[110:113]
	s_nop 2
	v_lshl_add_u64 v[112:113], v[108:109], 0, v[2:3]
	v_mfma_f32_16x16x32_bf16 v[96:99], v[138:141], v[130:133], v[114:117]
	v_lshlrev_b64 v[112:113], 12, v[112:113]
	v_cvt_pk_bf16_f32 v108, v146, v147
	v_cvt_pk_bf16_f32 v109, v148, v149
	v_lshl_add_u64 v[114:115], v[226:227], 1, s[54:55]
	v_lshl_add_u64 v[112:113], v[114:115], 0, v[112:113]
	v_cvt_pk_bf16_f32 v110, v150, v151
	v_cvt_pk_bf16_f32 v111, v152, v153
	v_add_co_u32_e32 v114, vcc, s58, v112
	v_mfma_f32_16x16x32_bf16 v[72:75], v[138:141], v[134:137], v[122:125]
	global_store_dwordx4 v[112:113], v[108:111], off
	v_addc_co_u32_e32 v115, vcc, 0, v113, vcc
	v_mfma_f32_16x16x32_bf16 v[68:71], v[142:145], v[134:137], v[126:129]
	v_cvt_pk_bf16_f32 v108, v104, v105
	v_cvt_pk_bf16_f32 v109, v106, v107
	v_cvt_pk_bf16_f32 v110, v100, v101
	v_cvt_pk_bf16_f32 v111, v102, v103
	global_store_dwordx4 v[114:115], v[108:111], off
	v_add_co_u32_e32 v114, vcc, s59, v112
	s_nop 0
	v_cvt_pk_bf16_f32 v108, v96, v97
	v_addc_co_u32_e32 v115, vcc, 0, v113, vcc
	v_cvt_pk_bf16_f32 v109, v98, v99
	v_cvt_pk_bf16_f32 v110, v92, v93
	v_cvt_pk_bf16_f32 v111, v94, v95
	v_add_co_u32_e32 v112, vcc, s0, v112
	global_store_dwordx4 v[114:115], v[108:111], off
	s_nop 0
	v_addc_co_u32_e32 v113, vcc, 0, v113, vcc
	v_cvt_pk_bf16_f32 v108, v72, v73
	v_cvt_pk_bf16_f32 v109, v74, v75
	v_cvt_pk_bf16_f32 v110, v68, v69
	v_cvt_pk_bf16_f32 v111, v70, v71
	global_store_dwordx4 v[112:113], v[108:111], off
	v_pk_mul_f32 v[112:113], v[146:147], v[146:147]
	v_pk_mul_f32 v[116:117], v[150:151], v[150:151]
	v_add_f32_e32 v110, 0, v146
	v_add_f32_e32 v110, v147, v110
	v_add_f32_e32 v115, v148, v110
	v_pk_mul_f32 v[110:111], v[148:149], v[148:149]
	v_fmac_f32_e32 v113, v146, v146
	v_add_f32_e32 v112, v110, v113
	v_add_f32_e32 v110, v149, v115
	v_mov_b32_e32 v148, v150
	v_add_f32_e32 v113, v150, v110
	v_pk_mul_f32 v[110:111], v[148:149], v[148:149]
	v_lshlrev_b32_e32 v108, 2, v230
	v_add_f32_e32 v111, v111, v112
	v_add_f32_e32 v111, v110, v111
	v_add_f32_e32 v110, v151, v113
	v_pk_mul_f32 v[112:113], v[152:153], v[152:153]
	v_add_f32_e32 v111, v117, v111
	v_add_f32_e32 v110, v152, v110
	v_add_f32_e32 v113, v112, v111
	v_mul_f32_e32 v111, v153, v153
	v_mov_b32_e32 v112, v153
	v_pk_add_f32 v[110:111], v[112:113], v[110:111]
	v_mov_b32_e32 v112, v110
	v_mov_b32_e32 v113, v111
	s_nop 1
	v_permlane16_swap_b32_e32 v112, v110
	v_permlane16_swap_b32_e32 v113, v111
	v_xor_b32_e32 v114, 0x80, v108
	v_lshl_add_u64 v[108:109], s[78:79], 0, v[230:231]
	v_lshl_add_u64 v[108:109], v[108:109], 0, v[228:229]
	v_lshl_add_u64 v[108:109], v[108:109], 0, s[60:61]
	s_waitcnt lgkmcnt(0)
	v_pk_add_f32 v[110:111], v[110:111], v[112:113]
	v_mov_b32_e32 v112, v110
	v_mov_b32_e32 v113, v111
	s_nop 1
	v_permlane32_swap_b32_e32 v112, v110
	v_permlane32_swap_b32_e32 v113, v111
	v_cmp_gt_u32_e32 vcc, 16, v230
	v_lshl_add_u64 v[108:109], v[108:109], 3, s[14:15]
	s_and_saveexec_b64 s[0:1], vcc
	s_cbranch_execz .LBB0_57
	s_waitcnt lgkmcnt(0)
	v_pk_add_f32 v[110:111], v[110:111], v[112:113]
	global_store_dwordx2 v[108:109], v[110:111], off
